# instruction selection (guide 7.5): MoE gate/up epilogue rows with packed f32 multiplies/adds and v_med3 clamp (same values)
# baseline (speedup 1.0000x reference)
.LBB0_1127:
	s_mov_b32 s14, 0
	s_lshl_b32 s14, s34, 2
	s_add_i32 s14, s3, s14
	v_mbcnt_lo_u32_b32 v146, -1, 0
	v_mbcnt_hi_u32_b32 v146, -1, v146
	v_mov_b32_e32 v128, s14
	ds_read2_b32 v[128:129], v128 offset0:64 offset1:224
	v_and_b32_e32 v143, 15, v146
	v_or_b32_e32 v144, s41, v143
	v_mov_b32_e32 v147, 0
	s_waitcnt lgkmcnt(0)
	v_lshlrev_b32_e32 v130, 2, v128
	v_add_u32_e32 v130, s3, v130
	ds_read_b32 v145, v130 offset:4
	v_ashrrev_i32_e32 v133, 31, v128
	v_mov_b32_e32 v132, v128
	v_add_u32_e32 v130, v129, v144
	v_lshlrev_b64 v[132:133], 16, v[132:133]
	s_waitcnt lgkmcnt(0)
	v_cmp_lt_i32_e32 vcc, v130, v145
	v_mov_b32_e32 v128, 0
	v_lshl_add_u64 v[132:133], s[10:11], 0, v[132:133]
	v_ashrrev_i32_e32 v131, 31, v130
	v_readlane_b32 s72, v249, 55
	v_readlane_b32 s73, v249, 56
	v_readlane_b32 s74, v249, 57
	v_readlane_b32 s75, v249, 58
	v_readlane_b32 s76, v249, 59
	v_readlane_b32 s77, v249, 60
	v_readlane_b32 s78, v249, 61
	v_readlane_b32 s79, v249, 62
	v_bfe_u32 v148, v146, 4, 2
	s_lshl_b32 s14, s64, 7
	v_lshl_add_u64 v[152:153], v[130:131], 2, v[132:133]
	v_lshl_or_b32 v149, v148, 3, s14
	global_load_dword v154, v[152:153], off
	global_load_dword v155, v[152:153], off offset:64
	global_load_dword v156, v[152:153], off offset:128
	global_load_dword v157, v[152:153], off offset:192
	global_load_dword v158, v[152:153], off offset:512
	global_load_dword v159, v[152:153], off offset:576
	global_load_dword v160, v[152:153], off offset:640
	global_load_dword v161, v[152:153], off offset:704
	s_lshl_b32 s14, s34, 8
	v_or_b32_e32 v149, s42, v149
	v_add_u32_e32 v150, s14, v144
	v_lshl_add_u32 v150, v150, 8, v149
	v_mov_b32_e32 v180, 0xbd38aa3b
	v_mov_b32_e32 v182, 0xc3e00000
	v_mov_b32_e32 v183, 0x43e00000
	v_cmp_lt_i32_e32 vcc, v130, v145
	s_waitcnt vmcnt(7)
	v_mul_f32_e32 v164, 0x3c800000, v154
	v_pk_mul_f32 v[166:167], v[124:125], v[180:181] op_sel_hi:[1,0]
	v_pk_mul_f32 v[168:169], v[126:127], v[180:181] op_sel_hi:[1,0]
	v_pk_mul_f32 v[170:171], v[116:117], v[180:181] op_sel_hi:[1,0]
	v_pk_mul_f32 v[172:173], v[118:119], v[180:181] op_sel_hi:[1,0]
	v_exp_f32_e32 v166, v166
	v_exp_f32_e32 v167, v167
	v_exp_f32_e32 v168, v168
	v_exp_f32_e32 v169, v169
	v_exp_f32_e32 v170, v170
	v_exp_f32_e32 v171, v171
	v_exp_f32_e32 v172, v172
	v_exp_f32_e32 v173, v173
	v_pk_add_f32 v[166:167], v[166:167], 1.0 op_sel_hi:[1,0]
	v_pk_add_f32 v[168:169], v[168:169], 1.0 op_sel_hi:[1,0]
	v_pk_add_f32 v[170:171], v[170:171], 1.0 op_sel_hi:[1,0]
	v_pk_add_f32 v[172:173], v[172:173], 1.0 op_sel_hi:[1,0]
	v_rcp_f32_e32 v166, v166
	v_rcp_f32_e32 v167, v167
	v_rcp_f32_e32 v168, v168
	v_rcp_f32_e32 v169, v169
	v_rcp_f32_e32 v170, v170
	v_rcp_f32_e32 v171, v171
	v_rcp_f32_e32 v172, v172
	v_rcp_f32_e32 v173, v173
	v_pk_mul_f32 v[166:167], v[124:125], v[166:167]
	v_pk_mul_f32 v[168:169], v[126:127], v[168:169]
	v_pk_mul_f32 v[170:171], v[116:117], v[170:171]
	v_pk_mul_f32 v[172:173], v[118:119], v[172:173]
	v_pk_mul_f32 v[166:167], v[166:167], v[120:121]
	v_pk_mul_f32 v[168:169], v[168:169], v[122:123]
	v_pk_mul_f32 v[170:171], v[170:171], v[112:113]
	v_pk_mul_f32 v[172:173], v[172:173], v[114:115]
	v_pk_mul_f32 v[166:167], v[166:167], v[164:165] op_sel_hi:[1,0]
	v_pk_mul_f32 v[168:169], v[168:169], v[164:165] op_sel_hi:[1,0]
	v_pk_mul_f32 v[170:171], v[170:171], v[164:165] op_sel_hi:[1,0]
	v_pk_mul_f32 v[172:173], v[172:173], v[164:165] op_sel_hi:[1,0]
	v_med3_f32 v166, v166, v182, v183
	v_med3_f32 v167, v167, v182, v183
	v_med3_f32 v168, v168, v182, v183
	v_med3_f32 v169, v169, v182, v183
	v_med3_f32 v170, v170, v182, v183
	v_med3_f32 v171, v171, v182, v183
	v_med3_f32 v172, v172, v182, v183
	v_med3_f32 v173, v173, v182, v183
	v_cndmask_b32_e32 v166, 0, v166, vcc
	v_cndmask_b32_e32 v167, 0, v167, vcc
	v_cndmask_b32_e32 v168, 0, v168, vcc
	v_cndmask_b32_e32 v169, 0, v169, vcc
	v_cndmask_b32_e32 v170, 0, v170, vcc
	v_cndmask_b32_e32 v171, 0, v171, vcc
	v_cndmask_b32_e32 v172, 0, v172, vcc
	v_cndmask_b32_e32 v173, 0, v173, vcc
	v_mov_b32_e32 v174, 0
	v_mov_b32_e32 v175, 0
	v_cvt_pk_fp8_f32 v174, v166, v167
	v_cvt_pk_fp8_f32 v175, v170, v171
	v_mov_b32_e32 v178, v150
	v_cvt_pk_fp8_f32 v174, v168, v169 op_sel:[0,0,1]
	v_cvt_pk_fp8_f32 v175, v172, v173 op_sel:[0,0,1]
	s_nop 1
	global_store_dwordx2 v178, v[174:175], s[12:13] sc1
	v_add_u32_e32 v162, 0x10, v130
	v_cmp_lt_i32_e32 vcc, v162, v145
	s_waitcnt vmcnt(7)
	v_mul_f32_e32 v164, 0x3c800000, v155
	v_pk_mul_f32 v[166:167], v[108:109], v[180:181] op_sel_hi:[1,0]
	v_pk_mul_f32 v[168:169], v[110:111], v[180:181] op_sel_hi:[1,0]
	v_pk_mul_f32 v[170:171], v[100:101], v[180:181] op_sel_hi:[1,0]
	v_pk_mul_f32 v[172:173], v[102:103], v[180:181] op_sel_hi:[1,0]
	v_exp_f32_e32 v166, v166
	v_exp_f32_e32 v167, v167
	v_exp_f32_e32 v168, v168
	v_exp_f32_e32 v169, v169
	v_exp_f32_e32 v170, v170
	v_exp_f32_e32 v171, v171
	v_exp_f32_e32 v172, v172
	v_exp_f32_e32 v173, v173
	v_pk_add_f32 v[166:167], v[166:167], 1.0 op_sel_hi:[1,0]
	v_pk_add_f32 v[168:169], v[168:169], 1.0 op_sel_hi:[1,0]
	v_pk_add_f32 v[170:171], v[170:171], 1.0 op_sel_hi:[1,0]
	v_pk_add_f32 v[172:173], v[172:173], 1.0 op_sel_hi:[1,0]
	v_rcp_f32_e32 v166, v166
	v_rcp_f32_e32 v167, v167
	v_rcp_f32_e32 v168, v168
	v_rcp_f32_e32 v169, v169
	v_rcp_f32_e32 v170, v170
	v_rcp_f32_e32 v171, v171
	v_rcp_f32_e32 v172, v172
	v_rcp_f32_e32 v173, v173
	v_pk_mul_f32 v[166:167], v[108:109], v[166:167]
	v_pk_mul_f32 v[168:169], v[110:111], v[168:169]
	v_pk_mul_f32 v[170:171], v[100:101], v[170:171]
	v_pk_mul_f32 v[172:173], v[102:103], v[172:173]
	v_pk_mul_f32 v[166:167], v[166:167], v[104:105]
	v_pk_mul_f32 v[168:169], v[168:169], v[106:107]
	v_pk_mul_f32 v[170:171], v[170:171], v[96:97]
	v_pk_mul_f32 v[172:173], v[172:173], v[98:99]
	v_pk_mul_f32 v[166:167], v[166:167], v[164:165] op_sel_hi:[1,0]
	v_pk_mul_f32 v[168:169], v[168:169], v[164:165] op_sel_hi:[1,0]
	v_pk_mul_f32 v[170:171], v[170:171], v[164:165] op_sel_hi:[1,0]
	v_pk_mul_f32 v[172:173], v[172:173], v[164:165] op_sel_hi:[1,0]
	v_med3_f32 v166, v166, v182, v183
	v_med3_f32 v167, v167, v182, v183
	v_med3_f32 v168, v168, v182, v183
	v_med3_f32 v169, v169, v182, v183
	v_med3_f32 v170, v170, v182, v183
	v_med3_f32 v171, v171, v182, v183
	v_med3_f32 v172, v172, v182, v183
	v_med3_f32 v173, v173, v182, v183
	v_cndmask_b32_e32 v166, 0, v166, vcc
	v_cndmask_b32_e32 v167, 0, v167, vcc
	v_cndmask_b32_e32 v168, 0, v168, vcc
	v_cndmask_b32_e32 v169, 0, v169, vcc
	v_cndmask_b32_e32 v170, 0, v170, vcc
	v_cndmask_b32_e32 v171, 0, v171, vcc
	v_cndmask_b32_e32 v172, 0, v172, vcc
	v_cndmask_b32_e32 v173, 0, v173, vcc
	v_mov_b32_e32 v176, 0
	v_mov_b32_e32 v177, 0
	v_cvt_pk_fp8_f32 v176, v166, v167
	v_cvt_pk_fp8_f32 v177, v170, v171
	v_add_u32_e32 v178, 0x1000, v150
	v_cvt_pk_fp8_f32 v176, v168, v169 op_sel:[0,0,1]
	v_cvt_pk_fp8_f32 v177, v172, v173 op_sel:[0,0,1]
	s_nop 1
	global_store_dwordx2 v178, v[176:177], s[12:13] sc1
	v_add_u32_e32 v162, 0x20, v130
	v_cmp_lt_i32_e32 vcc, v162, v145
	s_waitcnt vmcnt(7)
	v_mul_f32_e32 v164, 0x3c800000, v156
	v_pk_mul_f32 v[166:167], v[92:93], v[180:181] op_sel_hi:[1,0]
	v_pk_mul_f32 v[168:169], v[94:95], v[180:181] op_sel_hi:[1,0]
	v_pk_mul_f32 v[170:171], v[84:85], v[180:181] op_sel_hi:[1,0]
	v_pk_mul_f32 v[172:173], v[86:87], v[180:181] op_sel_hi:[1,0]
	v_exp_f32_e32 v166, v166
	v_exp_f32_e32 v167, v167
	v_exp_f32_e32 v168, v168
	v_exp_f32_e32 v169, v169
	v_exp_f32_e32 v170, v170
	v_exp_f32_e32 v171, v171
	v_exp_f32_e32 v172, v172
	v_exp_f32_e32 v173, v173
	v_pk_add_f32 v[166:167], v[166:167], 1.0 op_sel_hi:[1,0]
	v_pk_add_f32 v[168:169], v[168:169], 1.0 op_sel_hi:[1,0]
	v_pk_add_f32 v[170:171], v[170:171], 1.0 op_sel_hi:[1,0]
	v_pk_add_f32 v[172:173], v[172:173], 1.0 op_sel_hi:[1,0]
	v_rcp_f32_e32 v166, v166
	v_rcp_f32_e32 v167, v167
	v_rcp_f32_e32 v168, v168
	v_rcp_f32_e32 v169, v169
	v_rcp_f32_e32 v170, v170
	v_rcp_f32_e32 v171, v171
	v_rcp_f32_e32 v172, v172
	v_rcp_f32_e32 v173, v173
	v_pk_mul_f32 v[166:167], v[92:93], v[166:167]
	v_pk_mul_f32 v[168:169], v[94:95], v[168:169]
	v_pk_mul_f32 v[170:171], v[84:85], v[170:171]
	v_pk_mul_f32 v[172:173], v[86:87], v[172:173]
	v_pk_mul_f32 v[166:167], v[166:167], v[88:89]
	v_pk_mul_f32 v[168:169], v[168:169], v[90:91]
	v_pk_mul_f32 v[170:171], v[170:171], v[80:81]
	v_pk_mul_f32 v[172:173], v[172:173], v[82:83]
	v_pk_mul_f32 v[166:167], v[166:167], v[164:165] op_sel_hi:[1,0]
	v_pk_mul_f32 v[168:169], v[168:169], v[164:165] op_sel_hi:[1,0]
	v_pk_mul_f32 v[170:171], v[170:171], v[164:165] op_sel_hi:[1,0]
	v_pk_mul_f32 v[172:173], v[172:173], v[164:165] op_sel_hi:[1,0]
	v_med3_f32 v166, v166, v182, v183
	v_med3_f32 v167, v167, v182, v183
	v_med3_f32 v168, v168, v182, v183
	v_med3_f32 v169, v169, v182, v183
	v_med3_f32 v170, v170, v182, v183
	v_med3_f32 v171, v171, v182, v183
	v_med3_f32 v172, v172, v182, v183
	v_med3_f32 v173, v173, v182, v183
	v_cndmask_b32_e32 v166, 0, v166, vcc
	v_cndmask_b32_e32 v167, 0, v167, vcc
	v_cndmask_b32_e32 v168, 0, v168, vcc
	v_cndmask_b32_e32 v169, 0, v169, vcc
	v_cndmask_b32_e32 v170, 0, v170, vcc
	v_cndmask_b32_e32 v171, 0, v171, vcc
	v_cndmask_b32_e32 v172, 0, v172, vcc
	v_cndmask_b32_e32 v173, 0, v173, vcc
	v_mov_b32_e32 v174, 0
	v_mov_b32_e32 v175, 0
	v_cvt_pk_fp8_f32 v174, v166, v167
	v_cvt_pk_fp8_f32 v175, v170, v171
	v_add_u32_e32 v178, 0x2000, v150
	v_cvt_pk_fp8_f32 v174, v168, v169 op_sel:[0,0,1]
	v_cvt_pk_fp8_f32 v175, v172, v173 op_sel:[0,0,1]
	s_nop 1
	global_store_dwordx2 v178, v[174:175], s[12:13] sc1
	v_add_u32_e32 v162, 0x30, v130
	v_cmp_lt_i32_e32 vcc, v162, v145
	s_waitcnt vmcnt(7)
	v_mul_f32_e32 v164, 0x3c800000, v157
	v_pk_mul_f32 v[166:167], v[76:77], v[180:181] op_sel_hi:[1,0]
	v_pk_mul_f32 v[168:169], v[78:79], v[180:181] op_sel_hi:[1,0]
	v_pk_mul_f32 v[170:171], v[68:69], v[180:181] op_sel_hi:[1,0]
	v_pk_mul_f32 v[172:173], v[70:71], v[180:181] op_sel_hi:[1,0]
	v_exp_f32_e32 v166, v166
	v_exp_f32_e32 v167, v167
	v_exp_f32_e32 v168, v168
	v_exp_f32_e32 v169, v169
	v_exp_f32_e32 v170, v170
	v_exp_f32_e32 v171, v171
	v_exp_f32_e32 v172, v172
	v_exp_f32_e32 v173, v173
	v_pk_add_f32 v[166:167], v[166:167], 1.0 op_sel_hi:[1,0]
	v_pk_add_f32 v[168:169], v[168:169], 1.0 op_sel_hi:[1,0]
	v_pk_add_f32 v[170:171], v[170:171], 1.0 op_sel_hi:[1,0]
	v_pk_add_f32 v[172:173], v[172:173], 1.0 op_sel_hi:[1,0]
	v_rcp_f32_e32 v166, v166
	v_rcp_f32_e32 v167, v167
	v_rcp_f32_e32 v168, v168
	v_rcp_f32_e32 v169, v169
	v_rcp_f32_e32 v170, v170
	v_rcp_f32_e32 v171, v171
	v_rcp_f32_e32 v172, v172
	v_rcp_f32_e32 v173, v173
	v_pk_mul_f32 v[166:167], v[76:77], v[166:167]
	v_pk_mul_f32 v[168:169], v[78:79], v[168:169]
	v_pk_mul_f32 v[170:171], v[68:69], v[170:171]
	v_pk_mul_f32 v[172:173], v[70:71], v[172:173]
	v_pk_mul_f32 v[166:167], v[166:167], v[72:73]
	v_pk_mul_f32 v[168:169], v[168:169], v[74:75]
	v_pk_mul_f32 v[170:171], v[170:171], v[64:65]
	v_pk_mul_f32 v[172:173], v[172:173], v[66:67]
	v_pk_mul_f32 v[166:167], v[166:167], v[164:165] op_sel_hi:[1,0]
	v_pk_mul_f32 v[168:169], v[168:169], v[164:165] op_sel_hi:[1,0]
	v_pk_mul_f32 v[170:171], v[170:171], v[164:165] op_sel_hi:[1,0]
	v_pk_mul_f32 v[172:173], v[172:173], v[164:165] op_sel_hi:[1,0]
	v_med3_f32 v166, v166, v182, v183
	v_med3_f32 v167, v167, v182, v183
	v_med3_f32 v168, v168, v182, v183
	v_med3_f32 v169, v169, v182, v183
	v_med3_f32 v170, v170, v182, v183
	v_med3_f32 v171, v171, v182, v183
	v_med3_f32 v172, v172, v182, v183
	v_med3_f32 v173, v173, v182, v183
	v_cndmask_b32_e32 v166, 0, v166, vcc
	v_cndmask_b32_e32 v167, 0, v167, vcc
	v_cndmask_b32_e32 v168, 0, v168, vcc
	v_cndmask_b32_e32 v169, 0, v169, vcc
	v_cndmask_b32_e32 v170, 0, v170, vcc
	v_cndmask_b32_e32 v171, 0, v171, vcc
	v_cndmask_b32_e32 v172, 0, v172, vcc
	v_cndmask_b32_e32 v173, 0, v173, vcc
	v_mov_b32_e32 v176, 0
	v_mov_b32_e32 v177, 0
	v_cvt_pk_fp8_f32 v176, v166, v167
	v_cvt_pk_fp8_f32 v177, v170, v171
	v_add_u32_e32 v178, 0x3000, v150
	v_cvt_pk_fp8_f32 v176, v168, v169 op_sel:[0,0,1]
	v_cvt_pk_fp8_f32 v177, v172, v173 op_sel:[0,0,1]
	s_nop 1
	global_store_dwordx2 v178, v[176:177], s[12:13] sc1
	v_add_u32_e32 v162, 0x80, v130
	v_cmp_lt_i32_e32 vcc, v162, v145
	s_waitcnt vmcnt(7)
	v_mul_f32_e32 v164, 0x3c800000, v158
	v_pk_mul_f32 v[166:167], v[60:61], v[180:181] op_sel_hi:[1,0]
	v_pk_mul_f32 v[168:169], v[62:63], v[180:181] op_sel_hi:[1,0]
	v_pk_mul_f32 v[170:171], v[52:53], v[180:181] op_sel_hi:[1,0]
	v_pk_mul_f32 v[172:173], v[54:55], v[180:181] op_sel_hi:[1,0]
	v_exp_f32_e32 v166, v166
	v_exp_f32_e32 v167, v167
	v_exp_f32_e32 v168, v168
	v_exp_f32_e32 v169, v169
	v_exp_f32_e32 v170, v170
	v_exp_f32_e32 v171, v171
	v_exp_f32_e32 v172, v172
	v_exp_f32_e32 v173, v173
	v_pk_add_f32 v[166:167], v[166:167], 1.0 op_sel_hi:[1,0]
	v_pk_add_f32 v[168:169], v[168:169], 1.0 op_sel_hi:[1,0]
	v_pk_add_f32 v[170:171], v[170:171], 1.0 op_sel_hi:[1,0]
	v_pk_add_f32 v[172:173], v[172:173], 1.0 op_sel_hi:[1,0]
	v_rcp_f32_e32 v166, v166
	v_rcp_f32_e32 v167, v167
	v_rcp_f32_e32 v168, v168
	v_rcp_f32_e32 v169, v169
	v_rcp_f32_e32 v170, v170
	v_rcp_f32_e32 v171, v171
	v_rcp_f32_e32 v172, v172
	v_rcp_f32_e32 v173, v173
	v_pk_mul_f32 v[166:167], v[60:61], v[166:167]
	v_pk_mul_f32 v[168:169], v[62:63], v[168:169]
	v_pk_mul_f32 v[170:171], v[52:53], v[170:171]
	v_pk_mul_f32 v[172:173], v[54:55], v[172:173]
	v_pk_mul_f32 v[166:167], v[166:167], v[56:57]
	v_pk_mul_f32 v[168:169], v[168:169], v[58:59]
	v_pk_mul_f32 v[170:171], v[170:171], v[48:49]
	v_pk_mul_f32 v[172:173], v[172:173], v[50:51]
	v_pk_mul_f32 v[166:167], v[166:167], v[164:165] op_sel_hi:[1,0]
	v_pk_mul_f32 v[168:169], v[168:169], v[164:165] op_sel_hi:[1,0]
	v_pk_mul_f32 v[170:171], v[170:171], v[164:165] op_sel_hi:[1,0]
	v_pk_mul_f32 v[172:173], v[172:173], v[164:165] op_sel_hi:[1,0]
	v_med3_f32 v166, v166, v182, v183
	v_med3_f32 v167, v167, v182, v183
	v_med3_f32 v168, v168, v182, v183
	v_med3_f32 v169, v169, v182, v183
	v_med3_f32 v170, v170, v182, v183
	v_med3_f32 v171, v171, v182, v183
	v_med3_f32 v172, v172, v182, v183
	v_med3_f32 v173, v173, v182, v183
	v_cndmask_b32_e32 v166, 0, v166, vcc
	v_cndmask_b32_e32 v167, 0, v167, vcc
	v_cndmask_b32_e32 v168, 0, v168, vcc
	v_cndmask_b32_e32 v169, 0, v169, vcc
	v_cndmask_b32_e32 v170, 0, v170, vcc
	v_cndmask_b32_e32 v171, 0, v171, vcc
	v_cndmask_b32_e32 v172, 0, v172, vcc
	v_cndmask_b32_e32 v173, 0, v173, vcc
	v_mov_b32_e32 v174, 0
	v_mov_b32_e32 v175, 0
	v_cvt_pk_fp8_f32 v174, v166, v167
	v_cvt_pk_fp8_f32 v175, v170, v171
	v_add_u32_e32 v178, 0x8000, v150
	v_cvt_pk_fp8_f32 v174, v168, v169 op_sel:[0,0,1]
	v_cvt_pk_fp8_f32 v175, v172, v173 op_sel:[0,0,1]
	s_nop 1
	global_store_dwordx2 v178, v[174:175], s[12:13] sc1
	v_add_u32_e32 v162, 0x90, v130
	v_cmp_lt_i32_e32 vcc, v162, v145
	s_waitcnt vmcnt(7)
	v_mul_f32_e32 v164, 0x3c800000, v159
	v_pk_mul_f32 v[166:167], v[44:45], v[180:181] op_sel_hi:[1,0]
	v_pk_mul_f32 v[168:169], v[46:47], v[180:181] op_sel_hi:[1,0]
	v_pk_mul_f32 v[170:171], v[36:37], v[180:181] op_sel_hi:[1,0]
	v_pk_mul_f32 v[172:173], v[38:39], v[180:181] op_sel_hi:[1,0]
	v_exp_f32_e32 v166, v166
	v_exp_f32_e32 v167, v167
	v_exp_f32_e32 v168, v168
	v_exp_f32_e32 v169, v169
	v_exp_f32_e32 v170, v170
	v_exp_f32_e32 v171, v171
	v_exp_f32_e32 v172, v172
	v_exp_f32_e32 v173, v173
	v_pk_add_f32 v[166:167], v[166:167], 1.0 op_sel_hi:[1,0]
	v_pk_add_f32 v[168:169], v[168:169], 1.0 op_sel_hi:[1,0]
	v_pk_add_f32 v[170:171], v[170:171], 1.0 op_sel_hi:[1,0]
	v_pk_add_f32 v[172:173], v[172:173], 1.0 op_sel_hi:[1,0]
	v_rcp_f32_e32 v166, v166
	v_rcp_f32_e32 v167, v167
	v_rcp_f32_e32 v168, v168
	v_rcp_f32_e32 v169, v169
	v_rcp_f32_e32 v170, v170
	v_rcp_f32_e32 v171, v171
	v_rcp_f32_e32 v172, v172
	v_rcp_f32_e32 v173, v173
	v_pk_mul_f32 v[166:167], v[44:45], v[166:167]
	v_pk_mul_f32 v[168:169], v[46:47], v[168:169]
	v_pk_mul_f32 v[170:171], v[36:37], v[170:171]
	v_pk_mul_f32 v[172:173], v[38:39], v[172:173]
	v_pk_mul_f32 v[166:167], v[166:167], v[40:41]
	v_pk_mul_f32 v[168:169], v[168:169], v[42:43]
	v_pk_mul_f32 v[170:171], v[170:171], v[32:33]
	v_pk_mul_f32 v[172:173], v[172:173], v[34:35]
	v_pk_mul_f32 v[166:167], v[166:167], v[164:165] op_sel_hi:[1,0]
	v_pk_mul_f32 v[168:169], v[168:169], v[164:165] op_sel_hi:[1,0]
	v_pk_mul_f32 v[170:171], v[170:171], v[164:165] op_sel_hi:[1,0]
	v_pk_mul_f32 v[172:173], v[172:173], v[164:165] op_sel_hi:[1,0]
	v_med3_f32 v166, v166, v182, v183
	v_med3_f32 v167, v167, v182, v183
	v_med3_f32 v168, v168, v182, v183
	v_med3_f32 v169, v169, v182, v183
	v_med3_f32 v170, v170, v182, v183
	v_med3_f32 v171, v171, v182, v183
	v_med3_f32 v172, v172, v182, v183
	v_med3_f32 v173, v173, v182, v183
	v_cndmask_b32_e32 v166, 0, v166, vcc
	v_cndmask_b32_e32 v167, 0, v167, vcc
	v_cndmask_b32_e32 v168, 0, v168, vcc
	v_cndmask_b32_e32 v169, 0, v169, vcc
	v_cndmask_b32_e32 v170, 0, v170, vcc
	v_cndmask_b32_e32 v171, 0, v171, vcc
	v_cndmask_b32_e32 v172, 0, v172, vcc
	v_cndmask_b32_e32 v173, 0, v173, vcc
	v_mov_b32_e32 v176, 0
	v_mov_b32_e32 v177, 0
	v_cvt_pk_fp8_f32 v176, v166, v167
	v_cvt_pk_fp8_f32 v177, v170, v171
	v_add_u32_e32 v178, 0x9000, v150
	v_cvt_pk_fp8_f32 v176, v168, v169 op_sel:[0,0,1]
	v_cvt_pk_fp8_f32 v177, v172, v173 op_sel:[0,0,1]
	s_nop 1
	global_store_dwordx2 v178, v[176:177], s[12:13] sc1
	v_add_u32_e32 v162, 0xa0, v130
	v_cmp_lt_i32_e32 vcc, v162, v145
	s_waitcnt vmcnt(7)
	v_mul_f32_e32 v164, 0x3c800000, v160
	v_pk_mul_f32 v[166:167], v[28:29], v[180:181] op_sel_hi:[1,0]
	v_pk_mul_f32 v[168:169], v[30:31], v[180:181] op_sel_hi:[1,0]
	v_pk_mul_f32 v[170:171], v[20:21], v[180:181] op_sel_hi:[1,0]
	v_pk_mul_f32 v[172:173], v[22:23], v[180:181] op_sel_hi:[1,0]
	v_exp_f32_e32 v166, v166
	v_exp_f32_e32 v167, v167
	v_exp_f32_e32 v168, v168
	v_exp_f32_e32 v169, v169
	v_exp_f32_e32 v170, v170
	v_exp_f32_e32 v171, v171
	v_exp_f32_e32 v172, v172
	v_exp_f32_e32 v173, v173
	v_pk_add_f32 v[166:167], v[166:167], 1.0 op_sel_hi:[1,0]
	v_pk_add_f32 v[168:169], v[168:169], 1.0 op_sel_hi:[1,0]
	v_pk_add_f32 v[170:171], v[170:171], 1.0 op_sel_hi:[1,0]
	v_pk_add_f32 v[172:173], v[172:173], 1.0 op_sel_hi:[1,0]
	v_rcp_f32_e32 v166, v166
	v_rcp_f32_e32 v167, v167
	v_rcp_f32_e32 v168, v168
	v_rcp_f32_e32 v169, v169
	v_rcp_f32_e32 v170, v170
	v_rcp_f32_e32 v171, v171
	v_rcp_f32_e32 v172, v172
	v_rcp_f32_e32 v173, v173
	v_pk_mul_f32 v[166:167], v[28:29], v[166:167]
	v_pk_mul_f32 v[168:169], v[30:31], v[168:169]
	v_pk_mul_f32 v[170:171], v[20:21], v[170:171]
	v_pk_mul_f32 v[172:173], v[22:23], v[172:173]
	v_pk_mul_f32 v[166:167], v[166:167], v[24:25]
	v_pk_mul_f32 v[168:169], v[168:169], v[26:27]
	v_pk_mul_f32 v[170:171], v[170:171], v[16:17]
	v_pk_mul_f32 v[172:173], v[172:173], v[18:19]
	v_pk_mul_f32 v[166:167], v[166:167], v[164:165] op_sel_hi:[1,0]
	v_pk_mul_f32 v[168:169], v[168:169], v[164:165] op_sel_hi:[1,0]
	v_pk_mul_f32 v[170:171], v[170:171], v[164:165] op_sel_hi:[1,0]
	v_pk_mul_f32 v[172:173], v[172:173], v[164:165] op_sel_hi:[1,0]
	v_med3_f32 v166, v166, v182, v183
	v_med3_f32 v167, v167, v182, v183
	v_med3_f32 v168, v168, v182, v183
	v_med3_f32 v169, v169, v182, v183
	v_med3_f32 v170, v170, v182, v183
	v_med3_f32 v171, v171, v182, v183
	v_med3_f32 v172, v172, v182, v183
	v_med3_f32 v173, v173, v182, v183
	v_cndmask_b32_e32 v166, 0, v166, vcc
	v_cndmask_b32_e32 v167, 0, v167, vcc
	v_cndmask_b32_e32 v168, 0, v168, vcc
	v_cndmask_b32_e32 v169, 0, v169, vcc
	v_cndmask_b32_e32 v170, 0, v170, vcc
	v_cndmask_b32_e32 v171, 0, v171, vcc
	v_cndmask_b32_e32 v172, 0, v172, vcc
	v_cndmask_b32_e32 v173, 0, v173, vcc
	v_mov_b32_e32 v174, 0
	v_mov_b32_e32 v175, 0
	v_cvt_pk_fp8_f32 v174, v166, v167
	v_cvt_pk_fp8_f32 v175, v170, v171
	v_add_u32_e32 v178, 0xa000, v150
	v_cvt_pk_fp8_f32 v174, v168, v169 op_sel:[0,0,1]
	v_cvt_pk_fp8_f32 v175, v172, v173 op_sel:[0,0,1]
	s_nop 1
	global_store_dwordx2 v178, v[174:175], s[12:13] sc1
	v_add_u32_e32 v162, 0xb0, v130
	v_cmp_lt_i32_e32 vcc, v162, v145
	s_waitcnt vmcnt(7)
	v_mul_f32_e32 v164, 0x3c800000, v161
	v_pk_mul_f32 v[166:167], v[12:13], v[180:181] op_sel_hi:[1,0]
	v_pk_mul_f32 v[168:169], v[14:15], v[180:181] op_sel_hi:[1,0]
	v_pk_mul_f32 v[170:171], v[4:5], v[180:181] op_sel_hi:[1,0]
	v_pk_mul_f32 v[172:173], v[6:7], v[180:181] op_sel_hi:[1,0]
	v_exp_f32_e32 v166, v166
	v_exp_f32_e32 v167, v167
	v_exp_f32_e32 v168, v168
	v_exp_f32_e32 v169, v169
	v_exp_f32_e32 v170, v170
	v_exp_f32_e32 v171, v171
	v_exp_f32_e32 v172, v172
	v_exp_f32_e32 v173, v173
	v_pk_add_f32 v[166:167], v[166:167], 1.0 op_sel_hi:[1,0]
	v_pk_add_f32 v[168:169], v[168:169], 1.0 op_sel_hi:[1,0]
	v_pk_add_f32 v[170:171], v[170:171], 1.0 op_sel_hi:[1,0]
	v_pk_add_f32 v[172:173], v[172:173], 1.0 op_sel_hi:[1,0]
	v_rcp_f32_e32 v166, v166
	v_rcp_f32_e32 v167, v167
	v_rcp_f32_e32 v168, v168
	v_rcp_f32_e32 v169, v169
	v_rcp_f32_e32 v170, v170
	v_rcp_f32_e32 v171, v171
	v_rcp_f32_e32 v172, v172
	v_rcp_f32_e32 v173, v173
	v_pk_mul_f32 v[166:167], v[12:13], v[166:167]
	v_pk_mul_f32 v[168:169], v[14:15], v[168:169]
	v_pk_mul_f32 v[170:171], v[4:5], v[170:171]
	v_pk_mul_f32 v[172:173], v[6:7], v[172:173]
	v_pk_mul_f32 v[166:167], v[166:167], v[8:9]
	v_pk_mul_f32 v[168:169], v[168:169], v[10:11]
	v_pk_mul_f32 v[170:171], v[170:171], v[0:1]
	v_pk_mul_f32 v[172:173], v[172:173], v[2:3]
	v_pk_mul_f32 v[166:167], v[166:167], v[164:165] op_sel_hi:[1,0]
	v_pk_mul_f32 v[168:169], v[168:169], v[164:165] op_sel_hi:[1,0]
	v_pk_mul_f32 v[170:171], v[170:171], v[164:165] op_sel_hi:[1,0]
	v_pk_mul_f32 v[172:173], v[172:173], v[164:165] op_sel_hi:[1,0]
	v_med3_f32 v166, v166, v182, v183
	v_med3_f32 v167, v167, v182, v183
	v_med3_f32 v168, v168, v182, v183
	v_med3_f32 v169, v169, v182, v183
	v_med3_f32 v170, v170, v182, v183
	v_med3_f32 v171, v171, v182, v183
	v_med3_f32 v172, v172, v182, v183
	v_med3_f32 v173, v173, v182, v183
	v_cndmask_b32_e32 v166, 0, v166, vcc
	v_cndmask_b32_e32 v167, 0, v167, vcc
	v_cndmask_b32_e32 v168, 0, v168, vcc
	v_cndmask_b32_e32 v169, 0, v169, vcc
	v_cndmask_b32_e32 v170, 0, v170, vcc
	v_cndmask_b32_e32 v171, 0, v171, vcc
	v_cndmask_b32_e32 v172, 0, v172, vcc
	v_cndmask_b32_e32 v173, 0, v173, vcc
	v_mov_b32_e32 v176, 0
	v_mov_b32_e32 v177, 0
	v_cvt_pk_fp8_f32 v176, v166, v167
	v_cvt_pk_fp8_f32 v177, v170, v171
	v_add_u32_e32 v178, 0xb000, v150
	v_cvt_pk_fp8_f32 v176, v168, v169 op_sel:[0,0,1]
	v_cvt_pk_fp8_f32 v177, v172, v173 op_sel:[0,0,1]
	s_nop 1
	global_store_dwordx2 v178, v[176:177], s[12:13] sc1
	v_bfe_u32 v114, v146, 4, 2
	s_waitcnt vmcnt(0)
	v_or_b32_e32 v0, v114, v143
	v_cmp_eq_u32_e32 vcc, 0, v0
	s_and_saveexec_b64 s[22:23], vcc
	s_cbranch_execz .LBB0_1274
	s_mov_b64 s[24:25], exec
	v_mbcnt_lo_u32_b32 v0, s24, 0
	v_mbcnt_hi_u32_b32 v0, s25, v0
	v_cmp_eq_u32_e32 vcc, 0, v0
	s_and_b64 s[26:27], exec, vcc
	s_mov_b64 exec, s[26:27]
	s_cbranch_execz .LBB0_1274
	s_lshl_b32 s26, s34, 5
	s_ashr_i32 s27, s26, 31
	s_lshl_b64 s[26:27], s[26:27], 2
	s_add_u32 s26, s29, s26
	s_addc_u32 s27, s50, s27
	s_bcnt1_i32_b64 s14, s[24:25]
	s_lshl_b32 s14, s14, 1
	v_mov_b32_e32 v0, s14
	global_atomic_add v140, v0, s[26:27]

.LBB0_1289:
	s_lshl_b32 s0, s18, 2
	s_add_i32 s0, s3, s0
	v_mbcnt_lo_u32_b32 v72, -1, 0
	v_mbcnt_hi_u32_b32 v72, -1, v72
	v_mov_b32_e32 v64, s0
	ds_read2_b32 v[64:65], v64 offset0:64 offset1:224
	s_lshl_b32 s0, s20, 7
	v_and_b32_e32 v70, 15, v72
	s_add_i32 s0, s0, s24
	v_or_b32_e32 v71, s0, v70
	s_waitcnt lgkmcnt(0)
	v_ashrrev_i32_e32 v67, 31, v64
	v_mov_b32_e32 v66, v64
	v_lshlrev_b32_e32 v64, 2, v64
	v_add_u32_e32 v64, s3, v64
	ds_read_b32 v64, v64 offset:4
	v_lshlrev_b64 v[68:69], 16, v[66:67]
	v_add_u32_e32 v66, v65, v71
	v_mov_b32_e32 v73, 0
	v_lshl_add_u64 v[68:69], s[10:11], 0, v[68:69]
	s_waitcnt lgkmcnt(0)
	v_cmp_lt_i32_e32 vcc, v66, v64
	v_ashrrev_i32_e32 v67, 31, v66
	v_mov_b32_e32 v74, 0
	v_bfe_u32 v140, v72, 4, 2
	s_lshl_b32 s0, s19, 7
	v_lshl_add_u64 v[144:145], v[66:67], 2, v[68:69]
	v_lshl_or_b32 v141, v140, 3, s0
	global_load_dword v146, v[144:145], off
	global_load_dword v147, v[144:145], off offset:64
	global_load_dword v148, v[144:145], off offset:128
	global_load_dword v149, v[144:145], off offset:192
	s_lshl_b32 s4, s18, 8
	v_or_b32_e32 v141, s21, v141
	v_add_u32_e32 v142, s4, v71
	v_lshl_add_u32 v142, v142, 8, v141
	v_mov_b32_e32 v172, 0xbd38aa3b
	v_mov_b32_e32 v174, 0xc3e00000
	v_mov_b32_e32 v175, 0x43e00000
	v_cmp_lt_i32_e32 vcc, v66, v64
	s_waitcnt vmcnt(3)
	v_mul_f32_e32 v156, 0x3c800000, v146
	v_pk_mul_f32 v[158:159], v[60:61], v[172:173] op_sel_hi:[1,0]
	v_pk_mul_f32 v[160:161], v[62:63], v[172:173] op_sel_hi:[1,0]
	v_pk_mul_f32 v[162:163], v[52:53], v[172:173] op_sel_hi:[1,0]
	v_pk_mul_f32 v[164:165], v[54:55], v[172:173] op_sel_hi:[1,0]
	v_exp_f32_e32 v158, v158
	v_exp_f32_e32 v159, v159
	v_exp_f32_e32 v160, v160
	v_exp_f32_e32 v161, v161
	v_exp_f32_e32 v162, v162
	v_exp_f32_e32 v163, v163
	v_exp_f32_e32 v164, v164
	v_exp_f32_e32 v165, v165
	v_pk_add_f32 v[158:159], v[158:159], 1.0 op_sel_hi:[1,0]
	v_pk_add_f32 v[160:161], v[160:161], 1.0 op_sel_hi:[1,0]
	v_pk_add_f32 v[162:163], v[162:163], 1.0 op_sel_hi:[1,0]
	v_pk_add_f32 v[164:165], v[164:165], 1.0 op_sel_hi:[1,0]
	v_rcp_f32_e32 v158, v158
	v_rcp_f32_e32 v159, v159
	v_rcp_f32_e32 v160, v160
	v_rcp_f32_e32 v161, v161
	v_rcp_f32_e32 v162, v162
	v_rcp_f32_e32 v163, v163
	v_rcp_f32_e32 v164, v164
	v_rcp_f32_e32 v165, v165
	v_pk_mul_f32 v[158:159], v[60:61], v[158:159]
	v_pk_mul_f32 v[160:161], v[62:63], v[160:161]
	v_pk_mul_f32 v[162:163], v[52:53], v[162:163]
	v_pk_mul_f32 v[164:165], v[54:55], v[164:165]
	v_pk_mul_f32 v[158:159], v[158:159], v[56:57]
	v_pk_mul_f32 v[160:161], v[160:161], v[58:59]
	v_pk_mul_f32 v[162:163], v[162:163], v[48:49]
	v_pk_mul_f32 v[164:165], v[164:165], v[50:51]
	v_pk_mul_f32 v[158:159], v[158:159], v[156:157] op_sel_hi:[1,0]
	v_pk_mul_f32 v[160:161], v[160:161], v[156:157] op_sel_hi:[1,0]
	v_pk_mul_f32 v[162:163], v[162:163], v[156:157] op_sel_hi:[1,0]
	v_pk_mul_f32 v[164:165], v[164:165], v[156:157] op_sel_hi:[1,0]
	v_med3_f32 v158, v158, v174, v175
	v_med3_f32 v159, v159, v174, v175
	v_med3_f32 v160, v160, v174, v175
	v_med3_f32 v161, v161, v174, v175
	v_med3_f32 v162, v162, v174, v175
	v_med3_f32 v163, v163, v174, v175
	v_med3_f32 v164, v164, v174, v175
	v_med3_f32 v165, v165, v174, v175
	v_cndmask_b32_e32 v158, 0, v158, vcc
	v_cndmask_b32_e32 v159, 0, v159, vcc
	v_cndmask_b32_e32 v160, 0, v160, vcc
	v_cndmask_b32_e32 v161, 0, v161, vcc
	v_cndmask_b32_e32 v162, 0, v162, vcc
	v_cndmask_b32_e32 v163, 0, v163, vcc
	v_cndmask_b32_e32 v164, 0, v164, vcc
	v_cndmask_b32_e32 v165, 0, v165, vcc
	v_mov_b32_e32 v166, 0
	v_mov_b32_e32 v167, 0
	v_cvt_pk_fp8_f32 v166, v158, v159
	v_cvt_pk_fp8_f32 v167, v162, v163
	v_mov_b32_e32 v170, v142
	v_cvt_pk_fp8_f32 v166, v160, v161 op_sel:[0,0,1]
	v_cvt_pk_fp8_f32 v167, v164, v165 op_sel:[0,0,1]
	s_nop 1
	global_store_dwordx2 v170, v[166:167], s[12:13] sc1
	v_add_u32_e32 v154, 0x10, v66
	v_cmp_lt_i32_e32 vcc, v154, v64
	s_waitcnt vmcnt(3)
	v_mul_f32_e32 v156, 0x3c800000, v147
	v_pk_mul_f32 v[158:159], v[44:45], v[172:173] op_sel_hi:[1,0]
	v_pk_mul_f32 v[160:161], v[46:47], v[172:173] op_sel_hi:[1,0]
	v_pk_mul_f32 v[162:163], v[36:37], v[172:173] op_sel_hi:[1,0]
	v_pk_mul_f32 v[164:165], v[38:39], v[172:173] op_sel_hi:[1,0]
	v_exp_f32_e32 v158, v158
	v_exp_f32_e32 v159, v159
	v_exp_f32_e32 v160, v160
	v_exp_f32_e32 v161, v161
	v_exp_f32_e32 v162, v162
	v_exp_f32_e32 v163, v163
	v_exp_f32_e32 v164, v164
	v_exp_f32_e32 v165, v165
	v_pk_add_f32 v[158:159], v[158:159], 1.0 op_sel_hi:[1,0]
	v_pk_add_f32 v[160:161], v[160:161], 1.0 op_sel_hi:[1,0]
	v_pk_add_f32 v[162:163], v[162:163], 1.0 op_sel_hi:[1,0]
	v_pk_add_f32 v[164:165], v[164:165], 1.0 op_sel_hi:[1,0]
	v_rcp_f32_e32 v158, v158
	v_rcp_f32_e32 v159, v159
	v_rcp_f32_e32 v160, v160
	v_rcp_f32_e32 v161, v161
	v_rcp_f32_e32 v162, v162
	v_rcp_f32_e32 v163, v163
	v_rcp_f32_e32 v164, v164
	v_rcp_f32_e32 v165, v165
	v_pk_mul_f32 v[158:159], v[44:45], v[158:159]
	v_pk_mul_f32 v[160:161], v[46:47], v[160:161]
	v_pk_mul_f32 v[162:163], v[36:37], v[162:163]
	v_pk_mul_f32 v[164:165], v[38:39], v[164:165]
	v_pk_mul_f32 v[158:159], v[158:159], v[40:41]
	v_pk_mul_f32 v[160:161], v[160:161], v[42:43]
	v_pk_mul_f32 v[162:163], v[162:163], v[32:33]
	v_pk_mul_f32 v[164:165], v[164:165], v[34:35]
	v_pk_mul_f32 v[158:159], v[158:159], v[156:157] op_sel_hi:[1,0]
	v_pk_mul_f32 v[160:161], v[160:161], v[156:157] op_sel_hi:[1,0]
	v_pk_mul_f32 v[162:163], v[162:163], v[156:157] op_sel_hi:[1,0]
	v_pk_mul_f32 v[164:165], v[164:165], v[156:157] op_sel_hi:[1,0]
	v_med3_f32 v158, v158, v174, v175
	v_med3_f32 v159, v159, v174, v175
	v_med3_f32 v160, v160, v174, v175
	v_med3_f32 v161, v161, v174, v175
	v_med3_f32 v162, v162, v174, v175
	v_med3_f32 v163, v163, v174, v175
	v_med3_f32 v164, v164, v174, v175
	v_med3_f32 v165, v165, v174, v175
	v_cndmask_b32_e32 v158, 0, v158, vcc
	v_cndmask_b32_e32 v159, 0, v159, vcc
	v_cndmask_b32_e32 v160, 0, v160, vcc
	v_cndmask_b32_e32 v161, 0, v161, vcc
	v_cndmask_b32_e32 v162, 0, v162, vcc
	v_cndmask_b32_e32 v163, 0, v163, vcc
	v_cndmask_b32_e32 v164, 0, v164, vcc
	v_cndmask_b32_e32 v165, 0, v165, vcc
	v_mov_b32_e32 v168, 0
	v_mov_b32_e32 v169, 0
	v_cvt_pk_fp8_f32 v168, v158, v159
	v_cvt_pk_fp8_f32 v169, v162, v163
	v_add_u32_e32 v170, 0x1000, v142
	v_cvt_pk_fp8_f32 v168, v160, v161 op_sel:[0,0,1]
	v_cvt_pk_fp8_f32 v169, v164, v165 op_sel:[0,0,1]
	s_nop 1
	global_store_dwordx2 v170, v[168:169], s[12:13] sc1
	v_add_u32_e32 v154, 0x20, v66
	v_cmp_lt_i32_e32 vcc, v154, v64
	s_waitcnt vmcnt(3)
	v_mul_f32_e32 v156, 0x3c800000, v148
	v_pk_mul_f32 v[158:159], v[28:29], v[172:173] op_sel_hi:[1,0]
	v_pk_mul_f32 v[160:161], v[30:31], v[172:173] op_sel_hi:[1,0]
	v_pk_mul_f32 v[162:163], v[20:21], v[172:173] op_sel_hi:[1,0]
	v_pk_mul_f32 v[164:165], v[22:23], v[172:173] op_sel_hi:[1,0]
	v_exp_f32_e32 v158, v158
	v_exp_f32_e32 v159, v159
	v_exp_f32_e32 v160, v160
	v_exp_f32_e32 v161, v161
	v_exp_f32_e32 v162, v162
	v_exp_f32_e32 v163, v163
	v_exp_f32_e32 v164, v164
	v_exp_f32_e32 v165, v165
	v_pk_add_f32 v[158:159], v[158:159], 1.0 op_sel_hi:[1,0]
	v_pk_add_f32 v[160:161], v[160:161], 1.0 op_sel_hi:[1,0]
	v_pk_add_f32 v[162:163], v[162:163], 1.0 op_sel_hi:[1,0]
	v_pk_add_f32 v[164:165], v[164:165], 1.0 op_sel_hi:[1,0]
	v_rcp_f32_e32 v158, v158
	v_rcp_f32_e32 v159, v159
	v_rcp_f32_e32 v160, v160
	v_rcp_f32_e32 v161, v161
	v_rcp_f32_e32 v162, v162
	v_rcp_f32_e32 v163, v163
	v_rcp_f32_e32 v164, v164
	v_rcp_f32_e32 v165, v165
	v_pk_mul_f32 v[158:159], v[28:29], v[158:159]
	v_pk_mul_f32 v[160:161], v[30:31], v[160:161]
	v_pk_mul_f32 v[162:163], v[20:21], v[162:163]
	v_pk_mul_f32 v[164:165], v[22:23], v[164:165]
	v_pk_mul_f32 v[158:159], v[158:159], v[24:25]
	v_pk_mul_f32 v[160:161], v[160:161], v[26:27]
	v_pk_mul_f32 v[162:163], v[162:163], v[16:17]
	v_pk_mul_f32 v[164:165], v[164:165], v[18:19]
	v_pk_mul_f32 v[158:159], v[158:159], v[156:157] op_sel_hi:[1,0]
	v_pk_mul_f32 v[160:161], v[160:161], v[156:157] op_sel_hi:[1,0]
	v_pk_mul_f32 v[162:163], v[162:163], v[156:157] op_sel_hi:[1,0]
	v_pk_mul_f32 v[164:165], v[164:165], v[156:157] op_sel_hi:[1,0]
	v_med3_f32 v158, v158, v174, v175
	v_med3_f32 v159, v159, v174, v175
	v_med3_f32 v160, v160, v174, v175
	v_med3_f32 v161, v161, v174, v175
	v_med3_f32 v162, v162, v174, v175
	v_med3_f32 v163, v163, v174, v175
	v_med3_f32 v164, v164, v174, v175
	v_med3_f32 v165, v165, v174, v175
	v_cndmask_b32_e32 v158, 0, v158, vcc
	v_cndmask_b32_e32 v159, 0, v159, vcc
	v_cndmask_b32_e32 v160, 0, v160, vcc
	v_cndmask_b32_e32 v161, 0, v161, vcc
	v_cndmask_b32_e32 v162, 0, v162, vcc
	v_cndmask_b32_e32 v163, 0, v163, vcc
	v_cndmask_b32_e32 v164, 0, v164, vcc
	v_cndmask_b32_e32 v165, 0, v165, vcc
	v_mov_b32_e32 v166, 0
	v_mov_b32_e32 v167, 0
	v_cvt_pk_fp8_f32 v166, v158, v159
	v_cvt_pk_fp8_f32 v167, v162, v163
	v_add_u32_e32 v170, 0x2000, v142
	v_cvt_pk_fp8_f32 v166, v160, v161 op_sel:[0,0,1]
	v_cvt_pk_fp8_f32 v167, v164, v165 op_sel:[0,0,1]
	s_nop 1
	global_store_dwordx2 v170, v[166:167], s[12:13] sc1
	v_add_u32_e32 v154, 0x30, v66
	v_cmp_lt_i32_e32 vcc, v154, v64
	s_waitcnt vmcnt(3)
	v_mul_f32_e32 v156, 0x3c800000, v149
	v_pk_mul_f32 v[158:159], v[12:13], v[172:173] op_sel_hi:[1,0]
	v_pk_mul_f32 v[160:161], v[14:15], v[172:173] op_sel_hi:[1,0]
	v_pk_mul_f32 v[162:163], v[4:5], v[172:173] op_sel_hi:[1,0]
	v_pk_mul_f32 v[164:165], v[6:7], v[172:173] op_sel_hi:[1,0]
	v_exp_f32_e32 v158, v158
	v_exp_f32_e32 v159, v159
	v_exp_f32_e32 v160, v160
	v_exp_f32_e32 v161, v161
	v_exp_f32_e32 v162, v162
	v_exp_f32_e32 v163, v163
	v_exp_f32_e32 v164, v164
	v_exp_f32_e32 v165, v165
	v_pk_add_f32 v[158:159], v[158:159], 1.0 op_sel_hi:[1,0]
	v_pk_add_f32 v[160:161], v[160:161], 1.0 op_sel_hi:[1,0]
	v_pk_add_f32 v[162:163], v[162:163], 1.0 op_sel_hi:[1,0]
	v_pk_add_f32 v[164:165], v[164:165], 1.0 op_sel_hi:[1,0]
	v_rcp_f32_e32 v158, v158
	v_rcp_f32_e32 v159, v159
	v_rcp_f32_e32 v160, v160
	v_rcp_f32_e32 v161, v161
	v_rcp_f32_e32 v162, v162
	v_rcp_f32_e32 v163, v163
	v_rcp_f32_e32 v164, v164
	v_rcp_f32_e32 v165, v165
	v_pk_mul_f32 v[158:159], v[12:13], v[158:159]
	v_pk_mul_f32 v[160:161], v[14:15], v[160:161]
	v_pk_mul_f32 v[162:163], v[4:5], v[162:163]
	v_pk_mul_f32 v[164:165], v[6:7], v[164:165]
	v_pk_mul_f32 v[158:159], v[158:159], v[8:9]
	v_pk_mul_f32 v[160:161], v[160:161], v[10:11]
	v_pk_mul_f32 v[162:163], v[162:163], v[0:1]
	v_pk_mul_f32 v[164:165], v[164:165], v[2:3]
	v_pk_mul_f32 v[158:159], v[158:159], v[156:157] op_sel_hi:[1,0]
	v_pk_mul_f32 v[160:161], v[160:161], v[156:157] op_sel_hi:[1,0]
	v_pk_mul_f32 v[162:163], v[162:163], v[156:157] op_sel_hi:[1,0]
	v_pk_mul_f32 v[164:165], v[164:165], v[156:157] op_sel_hi:[1,0]
	v_med3_f32 v158, v158, v174, v175
	v_med3_f32 v159, v159, v174, v175
	v_med3_f32 v160, v160, v174, v175
	v_med3_f32 v161, v161, v174, v175
	v_med3_f32 v162, v162, v174, v175
	v_med3_f32 v163, v163, v174, v175
	v_med3_f32 v164, v164, v174, v175
	v_med3_f32 v165, v165, v174, v175
	v_cndmask_b32_e32 v158, 0, v158, vcc
	v_cndmask_b32_e32 v159, 0, v159, vcc
	v_cndmask_b32_e32 v160, 0, v160, vcc
	v_cndmask_b32_e32 v161, 0, v161, vcc
	v_cndmask_b32_e32 v162, 0, v162, vcc
	v_cndmask_b32_e32 v163, 0, v163, vcc
	v_cndmask_b32_e32 v164, 0, v164, vcc
	v_cndmask_b32_e32 v165, 0, v165, vcc
	v_mov_b32_e32 v168, 0
	v_mov_b32_e32 v169, 0
	v_cvt_pk_fp8_f32 v168, v158, v159
	v_cvt_pk_fp8_f32 v169, v162, v163
	v_add_u32_e32 v170, 0x3000, v142
	v_cvt_pk_fp8_f32 v168, v160, v161 op_sel:[0,0,1]
	v_cvt_pk_fp8_f32 v169, v164, v165 op_sel:[0,0,1]
	s_nop 1
	global_store_dwordx2 v170, v[168:169], s[12:13] sc1
	v_bfe_u32 v50, v72, 4, 2
	s_waitcnt vmcnt(0)
	v_or_b32_e32 v0, v50, v70
	v_cmp_eq_u32_e32 vcc, 0, v0
	s_and_saveexec_b64 s[0:1], vcc
	s_cbranch_execz .LBB0_1364
	s_mov_b64 s[4:5], exec
	v_mbcnt_lo_u32_b32 v0, s4, 0
	v_mbcnt_hi_u32_b32 v0, s5, v0
	v_cmp_eq_u32_e32 vcc, 0, v0
	s_and_b64 s[10:11], exec, vcc
	s_mov_b64 exec, s[10:11]
	s_cbranch_execz .LBB0_1364
	s_lshl_b32 s10, s18, 5
	s_ashr_i32 s11, s10, 31
	s_lshl_b64 s[10:11], s[10:11], 2
	s_add_u32 s10, s29, s10
	s_addc_u32 s11, s50, s11
	s_bcnt1_i32_b64 s4, s[4:5]
	v_mov_b32_e32 v0, 0
	v_mov_b32_e32 v1, s4
	global_atomic_add v0, v1, s[10:11]

.LBB0_2449:
	s_mov_b32 s14, 0
	s_lshl_b32 s14, s31, 2
	s_add_i32 s14, s3, s14
	v_mbcnt_lo_u32_b32 v146, -1, 0
	v_mbcnt_hi_u32_b32 v146, -1, v146
	v_mov_b32_e32 v128, s14
	ds_read2_b32 v[128:129], v128 offset0:64 offset1:224
	v_and_b32_e32 v143, 15, v146
	v_or_b32_e32 v144, s40, v143
	v_mov_b32_e32 v147, 0
	s_waitcnt lgkmcnt(0)
	v_lshlrev_b32_e32 v130, 2, v128
	v_add_u32_e32 v130, s3, v130
	ds_read_b32 v145, v130 offset:4
	v_ashrrev_i32_e32 v133, 31, v128
	v_mov_b32_e32 v132, v128
	v_add_u32_e32 v130, v129, v144
	v_lshlrev_b64 v[132:133], 16, v[132:133]
	s_waitcnt lgkmcnt(0)
	v_cmp_lt_i32_e32 vcc, v130, v145
	v_mov_b32_e32 v128, 0
	v_lshl_add_u64 v[132:133], s[10:11], 0, v[132:133]
	v_ashrrev_i32_e32 v131, 31, v130
	v_bfe_u32 v148, v146, 4, 2
	s_lshl_b32 s14, s56, 7
	v_lshl_add_u64 v[152:153], v[130:131], 2, v[132:133]
	v_lshl_or_b32 v149, v148, 3, s14
	global_load_dword v154, v[152:153], off
	global_load_dword v155, v[152:153], off offset:64
	global_load_dword v156, v[152:153], off offset:128
	global_load_dword v157, v[152:153], off offset:192
	global_load_dword v158, v[152:153], off offset:512
	global_load_dword v159, v[152:153], off offset:576
	global_load_dword v160, v[152:153], off offset:640
	global_load_dword v161, v[152:153], off offset:704
	s_lshl_b32 s14, s31, 8
	v_or_b32_e32 v149, s41, v149
	v_add_u32_e32 v150, s14, v144
	v_lshl_add_u32 v150, v150, 8, v149
	v_mov_b32_e32 v180, 0xbd38aa3b
	v_mov_b32_e32 v182, 0xc3e00000
	v_mov_b32_e32 v183, 0x43e00000
	v_cmp_lt_i32_e32 vcc, v130, v145
	s_waitcnt vmcnt(7)
	v_mul_f32_e32 v164, 0x3c800000, v154
	v_pk_mul_f32 v[166:167], v[124:125], v[180:181] op_sel_hi:[1,0]
	v_pk_mul_f32 v[168:169], v[126:127], v[180:181] op_sel_hi:[1,0]
	v_pk_mul_f32 v[170:171], v[116:117], v[180:181] op_sel_hi:[1,0]
	v_pk_mul_f32 v[172:173], v[118:119], v[180:181] op_sel_hi:[1,0]
	v_exp_f32_e32 v166, v166
	v_exp_f32_e32 v167, v167
	v_exp_f32_e32 v168, v168
	v_exp_f32_e32 v169, v169
	v_exp_f32_e32 v170, v170
	v_exp_f32_e32 v171, v171
	v_exp_f32_e32 v172, v172
	v_exp_f32_e32 v173, v173
	v_pk_add_f32 v[166:167], v[166:167], 1.0 op_sel_hi:[1,0]
	v_pk_add_f32 v[168:169], v[168:169], 1.0 op_sel_hi:[1,0]
	v_pk_add_f32 v[170:171], v[170:171], 1.0 op_sel_hi:[1,0]
	v_pk_add_f32 v[172:173], v[172:173], 1.0 op_sel_hi:[1,0]
	v_rcp_f32_e32 v166, v166
	v_rcp_f32_e32 v167, v167
	v_rcp_f32_e32 v168, v168
	v_rcp_f32_e32 v169, v169
	v_rcp_f32_e32 v170, v170
	v_rcp_f32_e32 v171, v171
	v_rcp_f32_e32 v172, v172
	v_rcp_f32_e32 v173, v173
	v_pk_mul_f32 v[166:167], v[124:125], v[166:167]
	v_pk_mul_f32 v[168:169], v[126:127], v[168:169]
	v_pk_mul_f32 v[170:171], v[116:117], v[170:171]
	v_pk_mul_f32 v[172:173], v[118:119], v[172:173]
	v_pk_mul_f32 v[166:167], v[166:167], v[120:121]
	v_pk_mul_f32 v[168:169], v[168:169], v[122:123]
	v_pk_mul_f32 v[170:171], v[170:171], v[112:113]
	v_pk_mul_f32 v[172:173], v[172:173], v[114:115]
	v_pk_mul_f32 v[166:167], v[166:167], v[164:165] op_sel_hi:[1,0]
	v_pk_mul_f32 v[168:169], v[168:169], v[164:165] op_sel_hi:[1,0]
	v_pk_mul_f32 v[170:171], v[170:171], v[164:165] op_sel_hi:[1,0]
	v_pk_mul_f32 v[172:173], v[172:173], v[164:165] op_sel_hi:[1,0]
	v_med3_f32 v166, v166, v182, v183
	v_med3_f32 v167, v167, v182, v183
	v_med3_f32 v168, v168, v182, v183
	v_med3_f32 v169, v169, v182, v183
	v_med3_f32 v170, v170, v182, v183
	v_med3_f32 v171, v171, v182, v183
	v_med3_f32 v172, v172, v182, v183
	v_med3_f32 v173, v173, v182, v183
	v_cndmask_b32_e32 v166, 0, v166, vcc
	v_cndmask_b32_e32 v167, 0, v167, vcc
	v_cndmask_b32_e32 v168, 0, v168, vcc
	v_cndmask_b32_e32 v169, 0, v169, vcc
	v_cndmask_b32_e32 v170, 0, v170, vcc
	v_cndmask_b32_e32 v171, 0, v171, vcc
	v_cndmask_b32_e32 v172, 0, v172, vcc
	v_cndmask_b32_e32 v173, 0, v173, vcc
	v_mov_b32_e32 v174, 0
	v_mov_b32_e32 v175, 0
	v_cvt_pk_fp8_f32 v174, v166, v167
	v_cvt_pk_fp8_f32 v175, v170, v171
	v_mov_b32_e32 v178, v150
	v_cvt_pk_fp8_f32 v174, v168, v169 op_sel:[0,0,1]
	v_cvt_pk_fp8_f32 v175, v172, v173 op_sel:[0,0,1]
	s_nop 1
	global_store_dwordx2 v178, v[174:175], s[12:13] sc1
	v_add_u32_e32 v162, 0x10, v130
	v_cmp_lt_i32_e32 vcc, v162, v145
	s_waitcnt vmcnt(7)
	v_mul_f32_e32 v164, 0x3c800000, v155
	v_pk_mul_f32 v[166:167], v[108:109], v[180:181] op_sel_hi:[1,0]
	v_pk_mul_f32 v[168:169], v[110:111], v[180:181] op_sel_hi:[1,0]
	v_pk_mul_f32 v[170:171], v[100:101], v[180:181] op_sel_hi:[1,0]
	v_pk_mul_f32 v[172:173], v[102:103], v[180:181] op_sel_hi:[1,0]
	v_exp_f32_e32 v166, v166
	v_exp_f32_e32 v167, v167
	v_exp_f32_e32 v168, v168
	v_exp_f32_e32 v169, v169
	v_exp_f32_e32 v170, v170
	v_exp_f32_e32 v171, v171
	v_exp_f32_e32 v172, v172
	v_exp_f32_e32 v173, v173
	v_pk_add_f32 v[166:167], v[166:167], 1.0 op_sel_hi:[1,0]
	v_pk_add_f32 v[168:169], v[168:169], 1.0 op_sel_hi:[1,0]
	v_pk_add_f32 v[170:171], v[170:171], 1.0 op_sel_hi:[1,0]
	v_pk_add_f32 v[172:173], v[172:173], 1.0 op_sel_hi:[1,0]
	v_rcp_f32_e32 v166, v166
	v_rcp_f32_e32 v167, v167
	v_rcp_f32_e32 v168, v168
	v_rcp_f32_e32 v169, v169
	v_rcp_f32_e32 v170, v170
	v_rcp_f32_e32 v171, v171
	v_rcp_f32_e32 v172, v172
	v_rcp_f32_e32 v173, v173
	v_pk_mul_f32 v[166:167], v[108:109], v[166:167]
	v_pk_mul_f32 v[168:169], v[110:111], v[168:169]
	v_pk_mul_f32 v[170:171], v[100:101], v[170:171]
	v_pk_mul_f32 v[172:173], v[102:103], v[172:173]
	v_pk_mul_f32 v[166:167], v[166:167], v[104:105]
	v_pk_mul_f32 v[168:169], v[168:169], v[106:107]
	v_pk_mul_f32 v[170:171], v[170:171], v[96:97]
	v_pk_mul_f32 v[172:173], v[172:173], v[98:99]
	v_pk_mul_f32 v[166:167], v[166:167], v[164:165] op_sel_hi:[1,0]
	v_pk_mul_f32 v[168:169], v[168:169], v[164:165] op_sel_hi:[1,0]
	v_pk_mul_f32 v[170:171], v[170:171], v[164:165] op_sel_hi:[1,0]
	v_pk_mul_f32 v[172:173], v[172:173], v[164:165] op_sel_hi:[1,0]
	v_med3_f32 v166, v166, v182, v183
	v_med3_f32 v167, v167, v182, v183
	v_med3_f32 v168, v168, v182, v183
	v_med3_f32 v169, v169, v182, v183
	v_med3_f32 v170, v170, v182, v183
	v_med3_f32 v171, v171, v182, v183
	v_med3_f32 v172, v172, v182, v183
	v_med3_f32 v173, v173, v182, v183
	v_cndmask_b32_e32 v166, 0, v166, vcc
	v_cndmask_b32_e32 v167, 0, v167, vcc
	v_cndmask_b32_e32 v168, 0, v168, vcc
	v_cndmask_b32_e32 v169, 0, v169, vcc
	v_cndmask_b32_e32 v170, 0, v170, vcc
	v_cndmask_b32_e32 v171, 0, v171, vcc
	v_cndmask_b32_e32 v172, 0, v172, vcc
	v_cndmask_b32_e32 v173, 0, v173, vcc
	v_mov_b32_e32 v176, 0
	v_mov_b32_e32 v177, 0
	v_cvt_pk_fp8_f32 v176, v166, v167
	v_cvt_pk_fp8_f32 v177, v170, v171
	v_add_u32_e32 v178, 0x1000, v150
	v_cvt_pk_fp8_f32 v176, v168, v169 op_sel:[0,0,1]
	v_cvt_pk_fp8_f32 v177, v172, v173 op_sel:[0,0,1]
	s_nop 1
	global_store_dwordx2 v178, v[176:177], s[12:13] sc1
	v_add_u32_e32 v162, 0x20, v130
	v_cmp_lt_i32_e32 vcc, v162, v145
	s_waitcnt vmcnt(7)
	v_mul_f32_e32 v164, 0x3c800000, v156
	v_pk_mul_f32 v[166:167], v[92:93], v[180:181] op_sel_hi:[1,0]
	v_pk_mul_f32 v[168:169], v[94:95], v[180:181] op_sel_hi:[1,0]
	v_pk_mul_f32 v[170:171], v[84:85], v[180:181] op_sel_hi:[1,0]
	v_pk_mul_f32 v[172:173], v[86:87], v[180:181] op_sel_hi:[1,0]
	v_exp_f32_e32 v166, v166
	v_exp_f32_e32 v167, v167
	v_exp_f32_e32 v168, v168
	v_exp_f32_e32 v169, v169
	v_exp_f32_e32 v170, v170
	v_exp_f32_e32 v171, v171
	v_exp_f32_e32 v172, v172
	v_exp_f32_e32 v173, v173
	v_pk_add_f32 v[166:167], v[166:167], 1.0 op_sel_hi:[1,0]
	v_pk_add_f32 v[168:169], v[168:169], 1.0 op_sel_hi:[1,0]
	v_pk_add_f32 v[170:171], v[170:171], 1.0 op_sel_hi:[1,0]
	v_pk_add_f32 v[172:173], v[172:173], 1.0 op_sel_hi:[1,0]
	v_rcp_f32_e32 v166, v166
	v_rcp_f32_e32 v167, v167
	v_rcp_f32_e32 v168, v168
	v_rcp_f32_e32 v169, v169
	v_rcp_f32_e32 v170, v170
	v_rcp_f32_e32 v171, v171
	v_rcp_f32_e32 v172, v172
	v_rcp_f32_e32 v173, v173
	v_pk_mul_f32 v[166:167], v[92:93], v[166:167]
	v_pk_mul_f32 v[168:169], v[94:95], v[168:169]
	v_pk_mul_f32 v[170:171], v[84:85], v[170:171]
	v_pk_mul_f32 v[172:173], v[86:87], v[172:173]
	v_pk_mul_f32 v[166:167], v[166:167], v[88:89]
	v_pk_mul_f32 v[168:169], v[168:169], v[90:91]
	v_pk_mul_f32 v[170:171], v[170:171], v[80:81]
	v_pk_mul_f32 v[172:173], v[172:173], v[82:83]
	v_pk_mul_f32 v[166:167], v[166:167], v[164:165] op_sel_hi:[1,0]
	v_pk_mul_f32 v[168:169], v[168:169], v[164:165] op_sel_hi:[1,0]
	v_pk_mul_f32 v[170:171], v[170:171], v[164:165] op_sel_hi:[1,0]
	v_pk_mul_f32 v[172:173], v[172:173], v[164:165] op_sel_hi:[1,0]
	v_med3_f32 v166, v166, v182, v183
	v_med3_f32 v167, v167, v182, v183
	v_med3_f32 v168, v168, v182, v183
	v_med3_f32 v169, v169, v182, v183
	v_med3_f32 v170, v170, v182, v183
	v_med3_f32 v171, v171, v182, v183
	v_med3_f32 v172, v172, v182, v183
	v_med3_f32 v173, v173, v182, v183
	v_cndmask_b32_e32 v166, 0, v166, vcc
	v_cndmask_b32_e32 v167, 0, v167, vcc
	v_cndmask_b32_e32 v168, 0, v168, vcc
	v_cndmask_b32_e32 v169, 0, v169, vcc
	v_cndmask_b32_e32 v170, 0, v170, vcc
	v_cndmask_b32_e32 v171, 0, v171, vcc
	v_cndmask_b32_e32 v172, 0, v172, vcc
	v_cndmask_b32_e32 v173, 0, v173, vcc
	v_mov_b32_e32 v174, 0
	v_mov_b32_e32 v175, 0
	v_cvt_pk_fp8_f32 v174, v166, v167
	v_cvt_pk_fp8_f32 v175, v170, v171
	v_add_u32_e32 v178, 0x2000, v150
	v_cvt_pk_fp8_f32 v174, v168, v169 op_sel:[0,0,1]
	v_cvt_pk_fp8_f32 v175, v172, v173 op_sel:[0,0,1]
	s_nop 1
	global_store_dwordx2 v178, v[174:175], s[12:13] sc1
	v_add_u32_e32 v162, 0x30, v130
	v_cmp_lt_i32_e32 vcc, v162, v145
	s_waitcnt vmcnt(7)
	v_mul_f32_e32 v164, 0x3c800000, v157
	v_pk_mul_f32 v[166:167], v[76:77], v[180:181] op_sel_hi:[1,0]
	v_pk_mul_f32 v[168:169], v[78:79], v[180:181] op_sel_hi:[1,0]
	v_pk_mul_f32 v[170:171], v[68:69], v[180:181] op_sel_hi:[1,0]
	v_pk_mul_f32 v[172:173], v[70:71], v[180:181] op_sel_hi:[1,0]
	v_exp_f32_e32 v166, v166
	v_exp_f32_e32 v167, v167
	v_exp_f32_e32 v168, v168
	v_exp_f32_e32 v169, v169
	v_exp_f32_e32 v170, v170
	v_exp_f32_e32 v171, v171
	v_exp_f32_e32 v172, v172
	v_exp_f32_e32 v173, v173
	v_pk_add_f32 v[166:167], v[166:167], 1.0 op_sel_hi:[1,0]
	v_pk_add_f32 v[168:169], v[168:169], 1.0 op_sel_hi:[1,0]
	v_pk_add_f32 v[170:171], v[170:171], 1.0 op_sel_hi:[1,0]
	v_pk_add_f32 v[172:173], v[172:173], 1.0 op_sel_hi:[1,0]
	v_rcp_f32_e32 v166, v166
	v_rcp_f32_e32 v167, v167
	v_rcp_f32_e32 v168, v168
	v_rcp_f32_e32 v169, v169
	v_rcp_f32_e32 v170, v170
	v_rcp_f32_e32 v171, v171
	v_rcp_f32_e32 v172, v172
	v_rcp_f32_e32 v173, v173
	v_pk_mul_f32 v[166:167], v[76:77], v[166:167]
	v_pk_mul_f32 v[168:169], v[78:79], v[168:169]
	v_pk_mul_f32 v[170:171], v[68:69], v[170:171]
	v_pk_mul_f32 v[172:173], v[70:71], v[172:173]
	v_pk_mul_f32 v[166:167], v[166:167], v[72:73]
	v_pk_mul_f32 v[168:169], v[168:169], v[74:75]
	v_pk_mul_f32 v[170:171], v[170:171], v[64:65]
	v_pk_mul_f32 v[172:173], v[172:173], v[66:67]
	v_pk_mul_f32 v[166:167], v[166:167], v[164:165] op_sel_hi:[1,0]
	v_pk_mul_f32 v[168:169], v[168:169], v[164:165] op_sel_hi:[1,0]
	v_pk_mul_f32 v[170:171], v[170:171], v[164:165] op_sel_hi:[1,0]
	v_pk_mul_f32 v[172:173], v[172:173], v[164:165] op_sel_hi:[1,0]
	v_med3_f32 v166, v166, v182, v183
	v_med3_f32 v167, v167, v182, v183
	v_med3_f32 v168, v168, v182, v183
	v_med3_f32 v169, v169, v182, v183
	v_med3_f32 v170, v170, v182, v183
	v_med3_f32 v171, v171, v182, v183
	v_med3_f32 v172, v172, v182, v183
	v_med3_f32 v173, v173, v182, v183
	v_cndmask_b32_e32 v166, 0, v166, vcc
	v_cndmask_b32_e32 v167, 0, v167, vcc
	v_cndmask_b32_e32 v168, 0, v168, vcc
	v_cndmask_b32_e32 v169, 0, v169, vcc
	v_cndmask_b32_e32 v170, 0, v170, vcc
	v_cndmask_b32_e32 v171, 0, v171, vcc
	v_cndmask_b32_e32 v172, 0, v172, vcc
	v_cndmask_b32_e32 v173, 0, v173, vcc
	v_mov_b32_e32 v176, 0
	v_mov_b32_e32 v177, 0
	v_cvt_pk_fp8_f32 v176, v166, v167
	v_cvt_pk_fp8_f32 v177, v170, v171
	v_add_u32_e32 v178, 0x3000, v150
	v_cvt_pk_fp8_f32 v176, v168, v169 op_sel:[0,0,1]
	v_cvt_pk_fp8_f32 v177, v172, v173 op_sel:[0,0,1]
	s_nop 1
	global_store_dwordx2 v178, v[176:177], s[12:13] sc1
	v_add_u32_e32 v162, 0x80, v130
	v_cmp_lt_i32_e32 vcc, v162, v145
	s_waitcnt vmcnt(7)
	v_mul_f32_e32 v164, 0x3c800000, v158
	v_pk_mul_f32 v[166:167], v[60:61], v[180:181] op_sel_hi:[1,0]
	v_pk_mul_f32 v[168:169], v[62:63], v[180:181] op_sel_hi:[1,0]
	v_pk_mul_f32 v[170:171], v[52:53], v[180:181] op_sel_hi:[1,0]
	v_pk_mul_f32 v[172:173], v[54:55], v[180:181] op_sel_hi:[1,0]
	v_exp_f32_e32 v166, v166
	v_exp_f32_e32 v167, v167
	v_exp_f32_e32 v168, v168
	v_exp_f32_e32 v169, v169
	v_exp_f32_e32 v170, v170
	v_exp_f32_e32 v171, v171
	v_exp_f32_e32 v172, v172
	v_exp_f32_e32 v173, v173
	v_pk_add_f32 v[166:167], v[166:167], 1.0 op_sel_hi:[1,0]
	v_pk_add_f32 v[168:169], v[168:169], 1.0 op_sel_hi:[1,0]
	v_pk_add_f32 v[170:171], v[170:171], 1.0 op_sel_hi:[1,0]
	v_pk_add_f32 v[172:173], v[172:173], 1.0 op_sel_hi:[1,0]
	v_rcp_f32_e32 v166, v166
	v_rcp_f32_e32 v167, v167
	v_rcp_f32_e32 v168, v168
	v_rcp_f32_e32 v169, v169
	v_rcp_f32_e32 v170, v170
	v_rcp_f32_e32 v171, v171
	v_rcp_f32_e32 v172, v172
	v_rcp_f32_e32 v173, v173
	v_pk_mul_f32 v[166:167], v[60:61], v[166:167]
	v_pk_mul_f32 v[168:169], v[62:63], v[168:169]
	v_pk_mul_f32 v[170:171], v[52:53], v[170:171]
	v_pk_mul_f32 v[172:173], v[54:55], v[172:173]
	v_pk_mul_f32 v[166:167], v[166:167], v[56:57]
	v_pk_mul_f32 v[168:169], v[168:169], v[58:59]
	v_pk_mul_f32 v[170:171], v[170:171], v[48:49]
	v_pk_mul_f32 v[172:173], v[172:173], v[50:51]
	v_pk_mul_f32 v[166:167], v[166:167], v[164:165] op_sel_hi:[1,0]
	v_pk_mul_f32 v[168:169], v[168:169], v[164:165] op_sel_hi:[1,0]
	v_pk_mul_f32 v[170:171], v[170:171], v[164:165] op_sel_hi:[1,0]
	v_pk_mul_f32 v[172:173], v[172:173], v[164:165] op_sel_hi:[1,0]
	v_med3_f32 v166, v166, v182, v183
	v_med3_f32 v167, v167, v182, v183
	v_med3_f32 v168, v168, v182, v183
	v_med3_f32 v169, v169, v182, v183
	v_med3_f32 v170, v170, v182, v183
	v_med3_f32 v171, v171, v182, v183
	v_med3_f32 v172, v172, v182, v183
	v_med3_f32 v173, v173, v182, v183
	v_cndmask_b32_e32 v166, 0, v166, vcc
	v_cndmask_b32_e32 v167, 0, v167, vcc
	v_cndmask_b32_e32 v168, 0, v168, vcc
	v_cndmask_b32_e32 v169, 0, v169, vcc
	v_cndmask_b32_e32 v170, 0, v170, vcc
	v_cndmask_b32_e32 v171, 0, v171, vcc
	v_cndmask_b32_e32 v172, 0, v172, vcc
	v_cndmask_b32_e32 v173, 0, v173, vcc
	v_mov_b32_e32 v174, 0
	v_mov_b32_e32 v175, 0
	v_cvt_pk_fp8_f32 v174, v166, v167
	v_cvt_pk_fp8_f32 v175, v170, v171
	v_add_u32_e32 v178, 0x8000, v150
	v_cvt_pk_fp8_f32 v174, v168, v169 op_sel:[0,0,1]
	v_cvt_pk_fp8_f32 v175, v172, v173 op_sel:[0,0,1]
	s_nop 1
	global_store_dwordx2 v178, v[174:175], s[12:13] sc1
	v_add_u32_e32 v162, 0x90, v130
	v_cmp_lt_i32_e32 vcc, v162, v145
	s_waitcnt vmcnt(7)
	v_mul_f32_e32 v164, 0x3c800000, v159
	v_pk_mul_f32 v[166:167], v[44:45], v[180:181] op_sel_hi:[1,0]
	v_pk_mul_f32 v[168:169], v[46:47], v[180:181] op_sel_hi:[1,0]
	v_pk_mul_f32 v[170:171], v[36:37], v[180:181] op_sel_hi:[1,0]
	v_pk_mul_f32 v[172:173], v[38:39], v[180:181] op_sel_hi:[1,0]
	v_exp_f32_e32 v166, v166
	v_exp_f32_e32 v167, v167
	v_exp_f32_e32 v168, v168
	v_exp_f32_e32 v169, v169
	v_exp_f32_e32 v170, v170
	v_exp_f32_e32 v171, v171
	v_exp_f32_e32 v172, v172
	v_exp_f32_e32 v173, v173
	v_pk_add_f32 v[166:167], v[166:167], 1.0 op_sel_hi:[1,0]
	v_pk_add_f32 v[168:169], v[168:169], 1.0 op_sel_hi:[1,0]
	v_pk_add_f32 v[170:171], v[170:171], 1.0 op_sel_hi:[1,0]
	v_pk_add_f32 v[172:173], v[172:173], 1.0 op_sel_hi:[1,0]
	v_rcp_f32_e32 v166, v166
	v_rcp_f32_e32 v167, v167
	v_rcp_f32_e32 v168, v168
	v_rcp_f32_e32 v169, v169
	v_rcp_f32_e32 v170, v170
	v_rcp_f32_e32 v171, v171
	v_rcp_f32_e32 v172, v172
	v_rcp_f32_e32 v173, v173
	v_pk_mul_f32 v[166:167], v[44:45], v[166:167]
	v_pk_mul_f32 v[168:169], v[46:47], v[168:169]
	v_pk_mul_f32 v[170:171], v[36:37], v[170:171]
	v_pk_mul_f32 v[172:173], v[38:39], v[172:173]
	v_pk_mul_f32 v[166:167], v[166:167], v[40:41]
	v_pk_mul_f32 v[168:169], v[168:169], v[42:43]
	v_pk_mul_f32 v[170:171], v[170:171], v[32:33]
	v_pk_mul_f32 v[172:173], v[172:173], v[34:35]
	v_pk_mul_f32 v[166:167], v[166:167], v[164:165] op_sel_hi:[1,0]
	v_pk_mul_f32 v[168:169], v[168:169], v[164:165] op_sel_hi:[1,0]
	v_pk_mul_f32 v[170:171], v[170:171], v[164:165] op_sel_hi:[1,0]
	v_pk_mul_f32 v[172:173], v[172:173], v[164:165] op_sel_hi:[1,0]
	v_med3_f32 v166, v166, v182, v183
	v_med3_f32 v167, v167, v182, v183
	v_med3_f32 v168, v168, v182, v183
	v_med3_f32 v169, v169, v182, v183
	v_med3_f32 v170, v170, v182, v183
	v_med3_f32 v171, v171, v182, v183
	v_med3_f32 v172, v172, v182, v183
	v_med3_f32 v173, v173, v182, v183
	v_cndmask_b32_e32 v166, 0, v166, vcc
	v_cndmask_b32_e32 v167, 0, v167, vcc
	v_cndmask_b32_e32 v168, 0, v168, vcc
	v_cndmask_b32_e32 v169, 0, v169, vcc
	v_cndmask_b32_e32 v170, 0, v170, vcc
	v_cndmask_b32_e32 v171, 0, v171, vcc
	v_cndmask_b32_e32 v172, 0, v172, vcc
	v_cndmask_b32_e32 v173, 0, v173, vcc
	v_mov_b32_e32 v176, 0
	v_mov_b32_e32 v177, 0
	v_cvt_pk_fp8_f32 v176, v166, v167
	v_cvt_pk_fp8_f32 v177, v170, v171
	v_add_u32_e32 v178, 0x9000, v150
	v_cvt_pk_fp8_f32 v176, v168, v169 op_sel:[0,0,1]
	v_cvt_pk_fp8_f32 v177, v172, v173 op_sel:[0,0,1]
	s_nop 1
	global_store_dwordx2 v178, v[176:177], s[12:13] sc1
	v_add_u32_e32 v162, 0xa0, v130
	v_cmp_lt_i32_e32 vcc, v162, v145
	s_waitcnt vmcnt(7)
	v_mul_f32_e32 v164, 0x3c800000, v160
	v_pk_mul_f32 v[166:167], v[28:29], v[180:181] op_sel_hi:[1,0]
	v_pk_mul_f32 v[168:169], v[30:31], v[180:181] op_sel_hi:[1,0]
	v_pk_mul_f32 v[170:171], v[20:21], v[180:181] op_sel_hi:[1,0]
	v_pk_mul_f32 v[172:173], v[22:23], v[180:181] op_sel_hi:[1,0]
	v_exp_f32_e32 v166, v166
	v_exp_f32_e32 v167, v167
	v_exp_f32_e32 v168, v168
	v_exp_f32_e32 v169, v169
	v_exp_f32_e32 v170, v170
	v_exp_f32_e32 v171, v171
	v_exp_f32_e32 v172, v172
	v_exp_f32_e32 v173, v173
	v_pk_add_f32 v[166:167], v[166:167], 1.0 op_sel_hi:[1,0]
	v_pk_add_f32 v[168:169], v[168:169], 1.0 op_sel_hi:[1,0]
	v_pk_add_f32 v[170:171], v[170:171], 1.0 op_sel_hi:[1,0]
	v_pk_add_f32 v[172:173], v[172:173], 1.0 op_sel_hi:[1,0]
	v_rcp_f32_e32 v166, v166
	v_rcp_f32_e32 v167, v167
	v_rcp_f32_e32 v168, v168
	v_rcp_f32_e32 v169, v169
	v_rcp_f32_e32 v170, v170
	v_rcp_f32_e32 v171, v171
	v_rcp_f32_e32 v172, v172
	v_rcp_f32_e32 v173, v173
	v_pk_mul_f32 v[166:167], v[28:29], v[166:167]
	v_pk_mul_f32 v[168:169], v[30:31], v[168:169]
	v_pk_mul_f32 v[170:171], v[20:21], v[170:171]
	v_pk_mul_f32 v[172:173], v[22:23], v[172:173]
	v_pk_mul_f32 v[166:167], v[166:167], v[24:25]
	v_pk_mul_f32 v[168:169], v[168:169], v[26:27]
	v_pk_mul_f32 v[170:171], v[170:171], v[16:17]
	v_pk_mul_f32 v[172:173], v[172:173], v[18:19]
	v_pk_mul_f32 v[166:167], v[166:167], v[164:165] op_sel_hi:[1,0]
	v_pk_mul_f32 v[168:169], v[168:169], v[164:165] op_sel_hi:[1,0]
	v_pk_mul_f32 v[170:171], v[170:171], v[164:165] op_sel_hi:[1,0]
	v_pk_mul_f32 v[172:173], v[172:173], v[164:165] op_sel_hi:[1,0]
	v_med3_f32 v166, v166, v182, v183
	v_med3_f32 v167, v167, v182, v183
	v_med3_f32 v168, v168, v182, v183
	v_med3_f32 v169, v169, v182, v183
	v_med3_f32 v170, v170, v182, v183
	v_med3_f32 v171, v171, v182, v183
	v_med3_f32 v172, v172, v182, v183
	v_med3_f32 v173, v173, v182, v183
	v_cndmask_b32_e32 v166, 0, v166, vcc
	v_cndmask_b32_e32 v167, 0, v167, vcc
	v_cndmask_b32_e32 v168, 0, v168, vcc
	v_cndmask_b32_e32 v169, 0, v169, vcc
	v_cndmask_b32_e32 v170, 0, v170, vcc
	v_cndmask_b32_e32 v171, 0, v171, vcc
	v_cndmask_b32_e32 v172, 0, v172, vcc
	v_cndmask_b32_e32 v173, 0, v173, vcc
	v_mov_b32_e32 v174, 0
	v_mov_b32_e32 v175, 0
	v_cvt_pk_fp8_f32 v174, v166, v167
	v_cvt_pk_fp8_f32 v175, v170, v171
	v_add_u32_e32 v178, 0xa000, v150
	v_cvt_pk_fp8_f32 v174, v168, v169 op_sel:[0,0,1]
	v_cvt_pk_fp8_f32 v175, v172, v173 op_sel:[0,0,1]
	s_nop 1
	global_store_dwordx2 v178, v[174:175], s[12:13] sc1
	v_add_u32_e32 v162, 0xb0, v130
	v_cmp_lt_i32_e32 vcc, v162, v145
	s_waitcnt vmcnt(7)
	v_mul_f32_e32 v164, 0x3c800000, v161
	v_pk_mul_f32 v[166:167], v[12:13], v[180:181] op_sel_hi:[1,0]
	v_pk_mul_f32 v[168:169], v[14:15], v[180:181] op_sel_hi:[1,0]
	v_pk_mul_f32 v[170:171], v[4:5], v[180:181] op_sel_hi:[1,0]
	v_pk_mul_f32 v[172:173], v[6:7], v[180:181] op_sel_hi:[1,0]
	v_exp_f32_e32 v166, v166
	v_exp_f32_e32 v167, v167
	v_exp_f32_e32 v168, v168
	v_exp_f32_e32 v169, v169
	v_exp_f32_e32 v170, v170
	v_exp_f32_e32 v171, v171
	v_exp_f32_e32 v172, v172
	v_exp_f32_e32 v173, v173
	v_pk_add_f32 v[166:167], v[166:167], 1.0 op_sel_hi:[1,0]
	v_pk_add_f32 v[168:169], v[168:169], 1.0 op_sel_hi:[1,0]
	v_pk_add_f32 v[170:171], v[170:171], 1.0 op_sel_hi:[1,0]
	v_pk_add_f32 v[172:173], v[172:173], 1.0 op_sel_hi:[1,0]
	v_rcp_f32_e32 v166, v166
	v_rcp_f32_e32 v167, v167
	v_rcp_f32_e32 v168, v168
	v_rcp_f32_e32 v169, v169
	v_rcp_f32_e32 v170, v170
	v_rcp_f32_e32 v171, v171
	v_rcp_f32_e32 v172, v172
	v_rcp_f32_e32 v173, v173
	v_pk_mul_f32 v[166:167], v[12:13], v[166:167]
	v_pk_mul_f32 v[168:169], v[14:15], v[168:169]
	v_pk_mul_f32 v[170:171], v[4:5], v[170:171]
	v_pk_mul_f32 v[172:173], v[6:7], v[172:173]
	v_pk_mul_f32 v[166:167], v[166:167], v[8:9]
	v_pk_mul_f32 v[168:169], v[168:169], v[10:11]
	v_pk_mul_f32 v[170:171], v[170:171], v[0:1]
	v_pk_mul_f32 v[172:173], v[172:173], v[2:3]
	v_pk_mul_f32 v[166:167], v[166:167], v[164:165] op_sel_hi:[1,0]
	v_pk_mul_f32 v[168:169], v[168:169], v[164:165] op_sel_hi:[1,0]
	v_pk_mul_f32 v[170:171], v[170:171], v[164:165] op_sel_hi:[1,0]
	v_pk_mul_f32 v[172:173], v[172:173], v[164:165] op_sel_hi:[1,0]
	v_med3_f32 v166, v166, v182, v183
	v_med3_f32 v167, v167, v182, v183
	v_med3_f32 v168, v168, v182, v183
	v_med3_f32 v169, v169, v182, v183
	v_med3_f32 v170, v170, v182, v183
	v_med3_f32 v171, v171, v182, v183
	v_med3_f32 v172, v172, v182, v183
	v_med3_f32 v173, v173, v182, v183
	v_cndmask_b32_e32 v166, 0, v166, vcc
	v_cndmask_b32_e32 v167, 0, v167, vcc
	v_cndmask_b32_e32 v168, 0, v168, vcc
	v_cndmask_b32_e32 v169, 0, v169, vcc
	v_cndmask_b32_e32 v170, 0, v170, vcc
	v_cndmask_b32_e32 v171, 0, v171, vcc
	v_cndmask_b32_e32 v172, 0, v172, vcc
	v_cndmask_b32_e32 v173, 0, v173, vcc
	v_mov_b32_e32 v176, 0
	v_mov_b32_e32 v177, 0
	v_cvt_pk_fp8_f32 v176, v166, v167
	v_cvt_pk_fp8_f32 v177, v170, v171
	v_add_u32_e32 v178, 0xb000, v150
	v_cvt_pk_fp8_f32 v176, v168, v169 op_sel:[0,0,1]
	v_cvt_pk_fp8_f32 v177, v172, v173 op_sel:[0,0,1]
	s_nop 1
	global_store_dwordx2 v178, v[176:177], s[12:13] sc1
	v_bfe_u32 v114, v146, 4, 2
	s_waitcnt vmcnt(0)
	v_or_b32_e32 v0, v114, v143
	v_cmp_eq_u32_e32 vcc, 0, v0
	s_and_saveexec_b64 s[22:23], vcc
	s_cbranch_execz .LBB0_2596
	s_mov_b64 s[24:25], exec
	v_mbcnt_lo_u32_b32 v0, s24, 0
	v_mbcnt_hi_u32_b32 v0, s25, v0
	v_cmp_eq_u32_e32 vcc, 0, v0
	s_and_b64 s[26:27], exec, vcc
	s_mov_b64 exec, s[26:27]
	s_cbranch_execz .LBB0_2596
	s_lshl_b32 s26, s31, 5
	s_ashr_i32 s27, s26, 31
	s_lshl_b64 s[26:27], s[26:27], 2
	s_add_u32 s26, s48, s26
	s_addc_u32 s27, s49, s27
	s_bcnt1_i32_b64 s14, s[24:25]
	s_lshl_b32 s14, s14, 1
	v_mov_b32_e32 v0, s14
	global_atomic_add v140, v0, s[26:27]

.LBB0_2611:
	s_lshl_b32 s0, s18, 2
	s_add_i32 s0, s3, s0
	v_mbcnt_lo_u32_b32 v72, -1, 0
	v_mbcnt_hi_u32_b32 v72, -1, v72
	v_mov_b32_e32 v64, s0
	ds_read2_b32 v[64:65], v64 offset0:64 offset1:224
	s_lshl_b32 s0, s20, 7
	v_and_b32_e32 v70, 15, v72
	s_add_i32 s0, s0, s24
	v_or_b32_e32 v71, s0, v70
	s_waitcnt lgkmcnt(0)
	v_ashrrev_i32_e32 v67, 31, v64
	v_mov_b32_e32 v66, v64
	v_lshlrev_b32_e32 v64, 2, v64
	v_add_u32_e32 v64, s3, v64
	ds_read_b32 v64, v64 offset:4
	v_lshlrev_b64 v[68:69], 16, v[66:67]
	v_add_u32_e32 v66, v65, v71
	v_mov_b32_e32 v73, 0
	v_lshl_add_u64 v[68:69], s[10:11], 0, v[68:69]
	s_waitcnt lgkmcnt(0)
	v_cmp_lt_i32_e32 vcc, v66, v64
	v_ashrrev_i32_e32 v67, 31, v66
	v_mov_b32_e32 v74, 0
	v_bfe_u32 v140, v72, 4, 2
	s_lshl_b32 s0, s19, 7
	v_lshl_add_u64 v[144:145], v[66:67], 2, v[68:69]
	v_lshl_or_b32 v141, v140, 3, s0
	global_load_dword v146, v[144:145], off
	global_load_dword v147, v[144:145], off offset:64
	global_load_dword v148, v[144:145], off offset:128
	global_load_dword v149, v[144:145], off offset:192
	s_lshl_b32 s4, s18, 8
	v_or_b32_e32 v141, s21, v141
	v_add_u32_e32 v142, s4, v71
	v_lshl_add_u32 v142, v142, 8, v141
	v_mov_b32_e32 v172, 0xbd38aa3b
	v_mov_b32_e32 v174, 0xc3e00000
	v_mov_b32_e32 v175, 0x43e00000
	v_cmp_lt_i32_e32 vcc, v66, v64
	s_waitcnt vmcnt(3)
	v_mul_f32_e32 v156, 0x3c800000, v146
	v_pk_mul_f32 v[158:159], v[60:61], v[172:173] op_sel_hi:[1,0]
	v_pk_mul_f32 v[160:161], v[62:63], v[172:173] op_sel_hi:[1,0]
	v_pk_mul_f32 v[162:163], v[52:53], v[172:173] op_sel_hi:[1,0]
	v_pk_mul_f32 v[164:165], v[54:55], v[172:173] op_sel_hi:[1,0]
	v_exp_f32_e32 v158, v158
	v_exp_f32_e32 v159, v159
	v_exp_f32_e32 v160, v160
	v_exp_f32_e32 v161, v161
	v_exp_f32_e32 v162, v162
	v_exp_f32_e32 v163, v163
	v_exp_f32_e32 v164, v164
	v_exp_f32_e32 v165, v165
	v_pk_add_f32 v[158:159], v[158:159], 1.0 op_sel_hi:[1,0]
	v_pk_add_f32 v[160:161], v[160:161], 1.0 op_sel_hi:[1,0]
	v_pk_add_f32 v[162:163], v[162:163], 1.0 op_sel_hi:[1,0]
	v_pk_add_f32 v[164:165], v[164:165], 1.0 op_sel_hi:[1,0]
	v_rcp_f32_e32 v158, v158
	v_rcp_f32_e32 v159, v159
	v_rcp_f32_e32 v160, v160
	v_rcp_f32_e32 v161, v161
	v_rcp_f32_e32 v162, v162
	v_rcp_f32_e32 v163, v163
	v_rcp_f32_e32 v164, v164
	v_rcp_f32_e32 v165, v165
	v_pk_mul_f32 v[158:159], v[60:61], v[158:159]
	v_pk_mul_f32 v[160:161], v[62:63], v[160:161]
	v_pk_mul_f32 v[162:163], v[52:53], v[162:163]
	v_pk_mul_f32 v[164:165], v[54:55], v[164:165]
	v_pk_mul_f32 v[158:159], v[158:159], v[56:57]
	v_pk_mul_f32 v[160:161], v[160:161], v[58:59]
	v_pk_mul_f32 v[162:163], v[162:163], v[48:49]
	v_pk_mul_f32 v[164:165], v[164:165], v[50:51]
	v_pk_mul_f32 v[158:159], v[158:159], v[156:157] op_sel_hi:[1,0]
	v_pk_mul_f32 v[160:161], v[160:161], v[156:157] op_sel_hi:[1,0]
	v_pk_mul_f32 v[162:163], v[162:163], v[156:157] op_sel_hi:[1,0]
	v_pk_mul_f32 v[164:165], v[164:165], v[156:157] op_sel_hi:[1,0]
	v_med3_f32 v158, v158, v174, v175
	v_med3_f32 v159, v159, v174, v175
	v_med3_f32 v160, v160, v174, v175
	v_med3_f32 v161, v161, v174, v175
	v_med3_f32 v162, v162, v174, v175
	v_med3_f32 v163, v163, v174, v175
	v_med3_f32 v164, v164, v174, v175
	v_med3_f32 v165, v165, v174, v175
	v_cndmask_b32_e32 v158, 0, v158, vcc
	v_cndmask_b32_e32 v159, 0, v159, vcc
	v_cndmask_b32_e32 v160, 0, v160, vcc
	v_cndmask_b32_e32 v161, 0, v161, vcc
	v_cndmask_b32_e32 v162, 0, v162, vcc
	v_cndmask_b32_e32 v163, 0, v163, vcc
	v_cndmask_b32_e32 v164, 0, v164, vcc
	v_cndmask_b32_e32 v165, 0, v165, vcc
	v_mov_b32_e32 v166, 0
	v_mov_b32_e32 v167, 0
	v_cvt_pk_fp8_f32 v166, v158, v159
	v_cvt_pk_fp8_f32 v167, v162, v163
	v_mov_b32_e32 v170, v142
	v_cvt_pk_fp8_f32 v166, v160, v161 op_sel:[0,0,1]
	v_cvt_pk_fp8_f32 v167, v164, v165 op_sel:[0,0,1]
	s_nop 1
	global_store_dwordx2 v170, v[166:167], s[12:13] sc1
	v_add_u32_e32 v154, 0x10, v66
	v_cmp_lt_i32_e32 vcc, v154, v64
	s_waitcnt vmcnt(3)
	v_mul_f32_e32 v156, 0x3c800000, v147
	v_pk_mul_f32 v[158:159], v[44:45], v[172:173] op_sel_hi:[1,0]
	v_pk_mul_f32 v[160:161], v[46:47], v[172:173] op_sel_hi:[1,0]
	v_pk_mul_f32 v[162:163], v[36:37], v[172:173] op_sel_hi:[1,0]
	v_pk_mul_f32 v[164:165], v[38:39], v[172:173] op_sel_hi:[1,0]
	v_exp_f32_e32 v158, v158
	v_exp_f32_e32 v159, v159
	v_exp_f32_e32 v160, v160
	v_exp_f32_e32 v161, v161
	v_exp_f32_e32 v162, v162
	v_exp_f32_e32 v163, v163
	v_exp_f32_e32 v164, v164
	v_exp_f32_e32 v165, v165
	v_pk_add_f32 v[158:159], v[158:159], 1.0 op_sel_hi:[1,0]
	v_pk_add_f32 v[160:161], v[160:161], 1.0 op_sel_hi:[1,0]
	v_pk_add_f32 v[162:163], v[162:163], 1.0 op_sel_hi:[1,0]
	v_pk_add_f32 v[164:165], v[164:165], 1.0 op_sel_hi:[1,0]
	v_rcp_f32_e32 v158, v158
	v_rcp_f32_e32 v159, v159
	v_rcp_f32_e32 v160, v160
	v_rcp_f32_e32 v161, v161
	v_rcp_f32_e32 v162, v162
	v_rcp_f32_e32 v163, v163
	v_rcp_f32_e32 v164, v164
	v_rcp_f32_e32 v165, v165
	v_pk_mul_f32 v[158:159], v[44:45], v[158:159]
	v_pk_mul_f32 v[160:161], v[46:47], v[160:161]
	v_pk_mul_f32 v[162:163], v[36:37], v[162:163]
	v_pk_mul_f32 v[164:165], v[38:39], v[164:165]
	v_pk_mul_f32 v[158:159], v[158:159], v[40:41]
	v_pk_mul_f32 v[160:161], v[160:161], v[42:43]
	v_pk_mul_f32 v[162:163], v[162:163], v[32:33]
	v_pk_mul_f32 v[164:165], v[164:165], v[34:35]
	v_pk_mul_f32 v[158:159], v[158:159], v[156:157] op_sel_hi:[1,0]
	v_pk_mul_f32 v[160:161], v[160:161], v[156:157] op_sel_hi:[1,0]
	v_pk_mul_f32 v[162:163], v[162:163], v[156:157] op_sel_hi:[1,0]
	v_pk_mul_f32 v[164:165], v[164:165], v[156:157] op_sel_hi:[1,0]
	v_med3_f32 v158, v158, v174, v175
	v_med3_f32 v159, v159, v174, v175
	v_med3_f32 v160, v160, v174, v175
	v_med3_f32 v161, v161, v174, v175
	v_med3_f32 v162, v162, v174, v175
	v_med3_f32 v163, v163, v174, v175
	v_med3_f32 v164, v164, v174, v175
	v_med3_f32 v165, v165, v174, v175
	v_cndmask_b32_e32 v158, 0, v158, vcc
	v_cndmask_b32_e32 v159, 0, v159, vcc
	v_cndmask_b32_e32 v160, 0, v160, vcc
	v_cndmask_b32_e32 v161, 0, v161, vcc
	v_cndmask_b32_e32 v162, 0, v162, vcc
	v_cndmask_b32_e32 v163, 0, v163, vcc
	v_cndmask_b32_e32 v164, 0, v164, vcc
	v_cndmask_b32_e32 v165, 0, v165, vcc
	v_mov_b32_e32 v168, 0
	v_mov_b32_e32 v169, 0
	v_cvt_pk_fp8_f32 v168, v158, v159
	v_cvt_pk_fp8_f32 v169, v162, v163
	v_add_u32_e32 v170, 0x1000, v142
	v_cvt_pk_fp8_f32 v168, v160, v161 op_sel:[0,0,1]
	v_cvt_pk_fp8_f32 v169, v164, v165 op_sel:[0,0,1]
	s_nop 1
	global_store_dwordx2 v170, v[168:169], s[12:13] sc1
	v_add_u32_e32 v154, 0x20, v66
	v_cmp_lt_i32_e32 vcc, v154, v64
	s_waitcnt vmcnt(3)
	v_mul_f32_e32 v156, 0x3c800000, v148
	v_pk_mul_f32 v[158:159], v[28:29], v[172:173] op_sel_hi:[1,0]
	v_pk_mul_f32 v[160:161], v[30:31], v[172:173] op_sel_hi:[1,0]
	v_pk_mul_f32 v[162:163], v[20:21], v[172:173] op_sel_hi:[1,0]
	v_pk_mul_f32 v[164:165], v[22:23], v[172:173] op_sel_hi:[1,0]
	v_exp_f32_e32 v158, v158
	v_exp_f32_e32 v159, v159
	v_exp_f32_e32 v160, v160
	v_exp_f32_e32 v161, v161
	v_exp_f32_e32 v162, v162
	v_exp_f32_e32 v163, v163
	v_exp_f32_e32 v164, v164
	v_exp_f32_e32 v165, v165
	v_pk_add_f32 v[158:159], v[158:159], 1.0 op_sel_hi:[1,0]
	v_pk_add_f32 v[160:161], v[160:161], 1.0 op_sel_hi:[1,0]
	v_pk_add_f32 v[162:163], v[162:163], 1.0 op_sel_hi:[1,0]
	v_pk_add_f32 v[164:165], v[164:165], 1.0 op_sel_hi:[1,0]
	v_rcp_f32_e32 v158, v158
	v_rcp_f32_e32 v159, v159
	v_rcp_f32_e32 v160, v160
	v_rcp_f32_e32 v161, v161
	v_rcp_f32_e32 v162, v162
	v_rcp_f32_e32 v163, v163
	v_rcp_f32_e32 v164, v164
	v_rcp_f32_e32 v165, v165
	v_pk_mul_f32 v[158:159], v[28:29], v[158:159]
	v_pk_mul_f32 v[160:161], v[30:31], v[160:161]
	v_pk_mul_f32 v[162:163], v[20:21], v[162:163]
	v_pk_mul_f32 v[164:165], v[22:23], v[164:165]
	v_pk_mul_f32 v[158:159], v[158:159], v[24:25]
	v_pk_mul_f32 v[160:161], v[160:161], v[26:27]
	v_pk_mul_f32 v[162:163], v[162:163], v[16:17]
	v_pk_mul_f32 v[164:165], v[164:165], v[18:19]
	v_pk_mul_f32 v[158:159], v[158:159], v[156:157] op_sel_hi:[1,0]
	v_pk_mul_f32 v[160:161], v[160:161], v[156:157] op_sel_hi:[1,0]
	v_pk_mul_f32 v[162:163], v[162:163], v[156:157] op_sel_hi:[1,0]
	v_pk_mul_f32 v[164:165], v[164:165], v[156:157] op_sel_hi:[1,0]
	v_med3_f32 v158, v158, v174, v175
	v_med3_f32 v159, v159, v174, v175
	v_med3_f32 v160, v160, v174, v175
	v_med3_f32 v161, v161, v174, v175
	v_med3_f32 v162, v162, v174, v175
	v_med3_f32 v163, v163, v174, v175
	v_med3_f32 v164, v164, v174, v175
	v_med3_f32 v165, v165, v174, v175
	v_cndmask_b32_e32 v158, 0, v158, vcc
	v_cndmask_b32_e32 v159, 0, v159, vcc
	v_cndmask_b32_e32 v160, 0, v160, vcc
	v_cndmask_b32_e32 v161, 0, v161, vcc
	v_cndmask_b32_e32 v162, 0, v162, vcc
	v_cndmask_b32_e32 v163, 0, v163, vcc
	v_cndmask_b32_e32 v164, 0, v164, vcc
	v_cndmask_b32_e32 v165, 0, v165, vcc
	v_mov_b32_e32 v166, 0
	v_mov_b32_e32 v167, 0
	v_cvt_pk_fp8_f32 v166, v158, v159
	v_cvt_pk_fp8_f32 v167, v162, v163
	v_add_u32_e32 v170, 0x2000, v142
	v_cvt_pk_fp8_f32 v166, v160, v161 op_sel:[0,0,1]
	v_cvt_pk_fp8_f32 v167, v164, v165 op_sel:[0,0,1]
	s_nop 1
	global_store_dwordx2 v170, v[166:167], s[12:13] sc1
	v_add_u32_e32 v154, 0x30, v66
	v_cmp_lt_i32_e32 vcc, v154, v64
	s_waitcnt vmcnt(3)
	v_mul_f32_e32 v156, 0x3c800000, v149
	v_pk_mul_f32 v[158:159], v[12:13], v[172:173] op_sel_hi:[1,0]
	v_pk_mul_f32 v[160:161], v[14:15], v[172:173] op_sel_hi:[1,0]
	v_pk_mul_f32 v[162:163], v[4:5], v[172:173] op_sel_hi:[1,0]
	v_pk_mul_f32 v[164:165], v[6:7], v[172:173] op_sel_hi:[1,0]
	v_exp_f32_e32 v158, v158
	v_exp_f32_e32 v159, v159
	v_exp_f32_e32 v160, v160
	v_exp_f32_e32 v161, v161
	v_exp_f32_e32 v162, v162
	v_exp_f32_e32 v163, v163
	v_exp_f32_e32 v164, v164
	v_exp_f32_e32 v165, v165
	v_pk_add_f32 v[158:159], v[158:159], 1.0 op_sel_hi:[1,0]
	v_pk_add_f32 v[160:161], v[160:161], 1.0 op_sel_hi:[1,0]
	v_pk_add_f32 v[162:163], v[162:163], 1.0 op_sel_hi:[1,0]
	v_pk_add_f32 v[164:165], v[164:165], 1.0 op_sel_hi:[1,0]
	v_rcp_f32_e32 v158, v158
	v_rcp_f32_e32 v159, v159
	v_rcp_f32_e32 v160, v160
	v_rcp_f32_e32 v161, v161
	v_rcp_f32_e32 v162, v162
	v_rcp_f32_e32 v163, v163
	v_rcp_f32_e32 v164, v164
	v_rcp_f32_e32 v165, v165
	v_pk_mul_f32 v[158:159], v[12:13], v[158:159]
	v_pk_mul_f32 v[160:161], v[14:15], v[160:161]
	v_pk_mul_f32 v[162:163], v[4:5], v[162:163]
	v_pk_mul_f32 v[164:165], v[6:7], v[164:165]
	v_pk_mul_f32 v[158:159], v[158:159], v[8:9]
	v_pk_mul_f32 v[160:161], v[160:161], v[10:11]
	v_pk_mul_f32 v[162:163], v[162:163], v[0:1]
	v_pk_mul_f32 v[164:165], v[164:165], v[2:3]
	v_pk_mul_f32 v[158:159], v[158:159], v[156:157] op_sel_hi:[1,0]
	v_pk_mul_f32 v[160:161], v[160:161], v[156:157] op_sel_hi:[1,0]
	v_pk_mul_f32 v[162:163], v[162:163], v[156:157] op_sel_hi:[1,0]
	v_pk_mul_f32 v[164:165], v[164:165], v[156:157] op_sel_hi:[1,0]
	v_med3_f32 v158, v158, v174, v175
	v_med3_f32 v159, v159, v174, v175
	v_med3_f32 v160, v160, v174, v175
	v_med3_f32 v161, v161, v174, v175
	v_med3_f32 v162, v162, v174, v175
	v_med3_f32 v163, v163, v174, v175
	v_med3_f32 v164, v164, v174, v175
	v_med3_f32 v165, v165, v174, v175
	v_cndmask_b32_e32 v158, 0, v158, vcc
	v_cndmask_b32_e32 v159, 0, v159, vcc
	v_cndmask_b32_e32 v160, 0, v160, vcc
	v_cndmask_b32_e32 v161, 0, v161, vcc
	v_cndmask_b32_e32 v162, 0, v162, vcc
	v_cndmask_b32_e32 v163, 0, v163, vcc
	v_cndmask_b32_e32 v164, 0, v164, vcc
	v_cndmask_b32_e32 v165, 0, v165, vcc
	v_mov_b32_e32 v168, 0
	v_mov_b32_e32 v169, 0
	v_cvt_pk_fp8_f32 v168, v158, v159
	v_cvt_pk_fp8_f32 v169, v162, v163
	v_add_u32_e32 v170, 0x3000, v142
	v_cvt_pk_fp8_f32 v168, v160, v161 op_sel:[0,0,1]
	v_cvt_pk_fp8_f32 v169, v164, v165 op_sel:[0,0,1]
	s_nop 1
	global_store_dwordx2 v170, v[168:169], s[12:13] sc1
	v_bfe_u32 v50, v72, 4, 2
	s_waitcnt vmcnt(0)
	v_or_b32_e32 v0, v50, v70
	v_cmp_eq_u32_e32 vcc, 0, v0
	s_and_saveexec_b64 s[0:1], vcc
	s_cbranch_execz .LBB0_2686
	s_mov_b64 s[4:5], exec
	v_mbcnt_lo_u32_b32 v0, s4, 0
	v_mbcnt_hi_u32_b32 v0, s5, v0
	v_cmp_eq_u32_e32 vcc, 0, v0
	s_and_b64 s[8:9], exec, vcc
	s_mov_b64 exec, s[8:9]
	s_cbranch_execz .LBB0_2686
	s_lshl_b32 s8, s18, 5
	s_ashr_i32 s9, s8, 31
	s_lshl_b64 s[8:9], s[8:9], 2
	s_add_u32 s8, s48, s8
	s_addc_u32 s9, s49, s9
	s_bcnt1_i32_b64 s4, s[4:5]
	v_mov_b32_e32 v0, 0
	v_mov_b32_e32 v1, s4
	global_atomic_add v0, v1, s[8:9]
